# gate_up epilogue sjobs pipelined across the unit boundary: second sjob issued after the 6th epilogue store, consumed at the end of the next unit's first K-loop trip
# speedup vs baseline: 1.0231x; 1.0009x over previous
; #define LAS __attribute__((address_space(3)))
; template <bool FP8, bool GATHER, class Epi, class Sched>
; __device__ __forceinline__ void gemm_phase(LAS unsigned char* lds, const Gemm g, const Sched& S, const Epi& E) {
;     const int tid = threadIdx.x, wid = __builtin_amdgcn_readfirstlane(tid >> 6), lane = tid & 63, wr = wid >> 2, wc = wid & 3, fr = lane & 15, fq = lane >> 4;
;     const int K = g.K, nt = K / BK;
;     unsigned voffA, voffB;
;     { int R, C; stage_rc(tid * 16, R, C); const int Rb = Epi::PERM ? ((R & ~31) + perm32(R & 31)) : R; voffA = (unsigned)(R * K + C) * 2u; voffB = (unsigned)(Rb * K + C) * 2u; }
;     const size_t pstep = (size_t)64 * K * 2;
;     unsigned voffC = 0, ro[4] = {0, 0, 0, 0}; int Rl = 0;
;     if constexpr (GATHER) { int R, C; stage_rc(tid * 16, R, C); voffC = (unsigned)C * 2u; Rl = R; }
;     ...
;     const size_t kstep = (size_t)(BK * 2);
;     const size_t hstep = (size_t)HALF * K * 2;
;     const size_t tstep = 2 * hstep;
;     const size_t estep = g.b_estride * 2;
;     const unsigned ldsw = (unsigned)wid * 1024u;
;     const int aoff0 = lds_byte(wr * 64 + fr, fq * 8), boff0 = lds_byte(wc * 32 + fr, fq * 8);
; __global__ void __launch_bounds__(512, 2) fwd(Args a) {
;     ...
;         pg8::Gemm g{(const bf16_t*)(a.ws + WS_H1), (const bf16_t*)(a.ws + WS_WGU_T), DM / 2, (size_t)4096 * 1024, (const LAS int*)(lds + LDS_ROWTAB)};
;         pg8::EpiGU8 E{a.b_gate_up, (unsigned char*)(a.ws + WS_ACT)};
;         g.probe = a.ws + 18688 + 32;
;         const int nmine = (((const LAS int*)(lds + LDS_EXTRA))[1] - (blk >> 3) + (G >> 3) - 1) / (G >> 3);
; #pragma unroll 1
;         for (int i0 = 0; i0 < (nmine > 0 ? nmine : 1); i0 += MAX_UNITS_WG) {
;             pg8::MoeOrder S{(const LAS int*)(lds + LDS_EXTRA), blk >> 3, G >> 3, i0, MAX_UNITS_WG};
.LBB0_827:
	s_or_b64 exec, exec, s[0:1]
	v_and_b32_e32 v254, 7, v0
	v_bfe_u32 v253, v0, 3, 3
	v_lshlrev_b32_e32 v252, 16, v254
	v_lshl_add_u32 v252, v253, 4, v252
	v_lshlrev_b32_e32 v253, 13, v253
	v_lshl_add_u32 v253, v254, 3, v253
	v_mov_b32_e32 v254, 0x3c800000
	v_readfirstlane_b32 s82, v0
	v_readlane_b32 s86, v255, 16
	v_readlane_b32 s87, v255, 17
	s_nop 3
	s_lshr_b32 s82, s82, 6
	s_lshl_b32 s84, s96, 3
	s_add_i32 s84, s84, s82
	s_lshl_b32 s83, s26, 3
	s_mov_b32 s98, 0
	s_mov_b32 s85, 0
	s_sub_u32 s86, s86, 0x30
	s_subb_u32 s87, s87, 0
	s_load_dwordx2 s[86:87], s[86:87], 0x0
	s_add_u32 s88, s74, 0x2b300000
	s_addc_u32 s89, s75, 0
	s_waitcnt lgkmcnt(0)
	s_mov_b32 s82, 0
	s_add_u32 s4, s74, 0x300000
	s_addc_u32 s5, s75, 0
	s_add_u32 s3, s74, 0xb300000
	s_addc_u32 s27, s75, 0
	s_add_u32 s8, s74, 0x55b00000
	s_addc_u32 s9, s75, 0
	s_add_i32 s0, 0, 0x20404
	s_ashr_i32 s47, s26, 3
	v_mov_b32_e32 v1, s0
	s_abs_i32 s0, s47
	v_cvt_f32_u32_e32 v3, s0
	s_waitcnt lgkmcnt(0)
	s_barrier
	ds_read_b32 v2, v1
	v_rcp_iflag_f32_e32 v3, v3
	s_ashr_i32 s50, s96, 3
	s_not_b32 s1, s50
	s_sub_i32 s10, 0, s0
	s_waitcnt lgkmcnt(0)
	v_readfirstlane_b32 s2, v2
	v_mul_f32_e32 v2, 0x4f7ffffe, v3
	v_cvt_u32_f32_e32 v2, v2
	s_add_i32 s1, s47, s1
	s_add_i32 s1, s1, s2
	s_xor_b32 s2, s1, s47
	v_readfirstlane_b32 s11, v2
	s_mul_i32 s10, s10, s11
	s_mul_hi_u32 s10, s11, s10
	s_abs_i32 s1, s1
	s_add_i32 s11, s11, s10
	s_mul_hi_u32 s10, s1, s11
	s_mul_i32 s11, s10, s0
	s_sub_i32 s1, s1, s11
	s_ashr_i32 s2, s2, 31
	s_add_i32 s11, s10, 1
	s_sub_i32 s12, s1, s0
	s_cmp_ge_u32 s1, s0
	s_cselect_b32 s10, s11, s10
	s_cselect_b32 s1, s12, s1
	s_add_i32 s11, s10, 1
	s_cmp_ge_u32 s1, s0
	s_cselect_b32 s0, s11, s10
	s_xor_b32 s0, s0, s2
	s_sub_i32 s0, s0, s2
	s_max_i32 s51, s0, 1
	v_lshlrev_b32_e32 v2, 4, v0
	v_and_b32_e32 v3, 32, v0
	s_add_u32 s52, s74, 0x5000
	v_lshrrev_b32_e32 v4, 3, v0
	v_bitop3_b32 v2, v2, v3, 48 bitop3:0x6c
	v_lshrrev_b32_e32 v3, 1, v0
	v_lshrrev_b32_e32 v5, 5, v0
	v_bfe_u32 v6, v0, 2, 2
	s_addc_u32 s53, s75, 0
	v_and_or_b32 v191, v0, 64, v2
	v_and_b32_e32 v2, 32, v4
	v_and_b32_e32 v4, 24, v3
	v_and_or_b32 v5, v5, 4, v6
	s_add_u32 s10, s74, 0x4b900000
	v_or3_b32 v2, v5, v2, v4
	v_lshlrev_b32_e32 v4, 6, v0
	v_lshlrev_b32_e32 v6, 2, v0
	s_addc_u32 s11, s75, 0
	s_add_i32 s0, 0, 0x21400
	v_lshl_or_b32 v178, v2, 11, v191
	v_and_b32_e32 v2, 48, v0
	v_and_b32_e32 v5, 0x3c0, v4
	v_and_b32_e32 v192, 32, v6
	v_and_b32_e32 v189, 0xff, v0
	s_movk_i32 s1, 0x3c0
	v_bitop3_b32 v193, v5, v192, v2 bitop3:0x36
	v_and_b32_e32 v3, 0xc0, v3
	v_and_b32_e32 v5, 60, v0
	v_mov_b32_e32 v181, 0
	s_add_u32 s12, s74, 0x300080
	s_mov_b32 s46, 0
	v_lshrrev_b32_e32 v188, 8, v0
	v_lshl_add_u32 v190, v189, 2, s0
	v_add3_u32 v194, s0, v3, v5
	v_mov_b32_e32 v179, v181
	s_addc_u32 s13, s75, 0
	s_add_i32 s54, 0, 0x20400
	s_add_i32 s55, 0, 0x20430
	s_movk_i32 s56, 0x2000
	v_and_or_b32 v195, v4, s1, v2
	s_mov_b64 s[14:15], 0x2000
	s_mov_b32 s57, 0xc0e00000
	s_mov_b32 s58, 0x40000
	s_mov_b32 s59, 0x48000
	s_mov_b32 s60, 0x50000
	v_mov_b32_e32 v196, 0x40e00000
	s_branch .LBB0_830

; __device__ __forceinline__ unsigned pk4_fp8(float a, float b, float c, float d) { int p = __builtin_amdgcn_cvt_pk_fp8_f32(a, b, 0, false); p = __builtin_amdgcn_cvt_pk_fp8_f32(c, d, p, true); return (unsigned)p; }
;     __device__ __forceinline__ void operator()(const f32x4 (&acc)[2][2][4][2], const Unit& u, int wr, int wc, int fr, int fq) const {
;     ...
;         for (int ai = 0; ai < 2; ++ai)
; #pragma unroll
;             for (int m = 0; m < 4; ++m) { float r[8];
; #pragma unroll
;                 for (int n = 0; n < 2; ++n)
; #pragma unroll
;                     for (int j = 0; j < 4; ++j) {
;                         float g = acc[ai][0][m][n][j] * W8_INV + bg[n][j], uu = acc[ai][1][m][n][j] * W8_INV + bu[n][j];
;                         g = fminf(g, 7.0f); uu = fminf(fmaxf(uu, -7.0f), 7.0f);
;                         const float glu = g * __builtin_amdgcn_rcpf(1.0f + __expf(-1.702f * g));
;                         r[n * 4 + j] = (uu + 1.0f) * glu; }
;                 u32x2 w; w.x = pk4_fp8(r[0], r[1], r[2], r[3]); w.y = pk4_fp8(r[4], r[5], r[6], r[7]);
;                 *(u32x2*)(O + (size_t)(row0 + ai * HALF + m * 16) * DM + cc) = w; }
.Lesj_join:
	v_fmamk_f32 v19, v175, 0x3c800000, v15
	v_fmamk_f32 v25, v166, 0x3c800000, v6
	v_min_f32_e32 v19, 0x40e00000, v19
	v_min_f32_e32 v25, 0x40e00000, v25
	v_fmamk_f32 v23, v176, 0x3c800000, v16
	v_mul_f32_e32 v36, 0xbfd9db23, v19
	v_mul_f32_e32 v39, 0xbfd9db23, v25
	v_min_f32_e32 v23, 0x40e00000, v23
	v_mul_f32_e32 v36, 0x3fb8aa3b, v36
	v_mul_f32_e32 v39, 0x3fb8aa3b, v39
	v_mul_f32_e32 v37, 0xbfd9db23, v23
	v_exp_f32_e32 v36, v36
	v_exp_f32_e32 v39, v39
	v_mul_f32_e32 v37, 0x3fb8aa3b, v37
	v_fmamk_f32 v18, v174, 0x3c800000, v14
	v_fmamk_f32 v24, v177, 0x3c800000, v17
	v_exp_f32_e32 v37, v37
	v_min_f32_e32 v18, 0x40e00000, v18
	v_min_f32_e32 v24, 0x40e00000, v24
	v_mul_f32_e32 v35, 0xbfd9db23, v18
	v_mul_f32_e32 v38, 0xbfd9db23, v24
	v_add_f32_e32 v36, 1.0, v36
	v_add_f32_e32 v39, 1.0, v39
	v_mul_f32_e32 v35, 0x3fb8aa3b, v35
	v_mul_f32_e32 v38, 0x3fb8aa3b, v38
	v_rcp_f32_e32 v36, v36
	v_rcp_f32_e32 v39, v39
	v_exp_f32_e32 v35, v35
	v_exp_f32_e32 v38, v38
	v_add_f32_e32 v37, 1.0, v37
	v_fmamk_f32 v27, v168, 0x3c800000, v8
	v_fmamk_f32 v29, v171, 0x3c800000, v11
	v_fmamk_f32 v32, v162, 0x3c800000, v2
	v_rcp_f32_e32 v37, v37
	v_min_f32_e32 v27, 0x40e00000, v27
	v_med3_f32 v29, v29, s57, v196
	v_med3_f32 v32, v32, s57, v196
	v_fmamk_f32 v26, v167, 0x3c800000, v7
	v_fmamk_f32 v30, v172, 0x3c800000, v12
	v_mul_f32_e32 v41, 0xbfd9db23, v27
	v_add_f32_e32 v29, 1.0, v29
	v_add_f32_e32 v32, 1.0, v32
	v_mul_f32_e32 v19, v19, v36
	v_mul_f32_e32 v25, v25, v39
	v_min_f32_e32 v26, 0x40e00000, v26
	v_med3_f32 v30, v30, s57, v196
	v_mul_f32_e32 v41, 0x3fb8aa3b, v41
	v_add_f32_e32 v35, 1.0, v35
	v_add_f32_e32 v38, 1.0, v38
	v_mul_f32_e32 v19, v29, v19
	v_mul_f32_e32 v29, v32, v25
	v_fmamk_f32 v25, v169, 0x3c800000, v9
	v_mul_f32_e32 v40, 0xbfd9db23, v26
	v_add_f32_e32 v30, 1.0, v30
	v_exp_f32_e32 v41, v41
	v_rcp_f32_e32 v35, v35
	v_rcp_f32_e32 v38, v38
	v_mul_f32_e32 v23, v23, v37
	v_min_f32_e32 v25, 0x40e00000, v25
	v_mul_f32_e32 v40, 0x3fb8aa3b, v40
	v_mul_f32_e32 v23, v30, v23
	v_mul_f32_e32 v30, 0xbfd9db23, v25
	v_fmamk_f32 v28, v170, 0x3c800000, v10
	v_fmamk_f32 v31, v173, 0x3c800000, v13
	v_exp_f32_e32 v40, v40
	v_mul_f32_e32 v30, 0x3fb8aa3b, v30
	v_med3_f32 v28, v28, s57, v196
	v_med3_f32 v31, v31, s57, v196
	v_exp_f32_e32 v30, v30
	v_add_f32_e32 v28, 1.0, v28
	v_add_f32_e32 v31, 1.0, v31
	v_add_f32_e32 v41, 1.0, v41
	v_mul_f32_e32 v18, v18, v35
	v_mul_f32_e32 v24, v24, v38
	v_mul_f32_e32 v18, v28, v18
	v_mul_f32_e32 v28, v31, v24
	v_rcp_f32_e32 v24, v41
	v_add_f32_e32 v40, 1.0, v40
	v_fmamk_f32 v34, v164, 0x3c800000, v4
	v_rcp_f32_e32 v40, v40
	v_add_f32_e32 v30, 1.0, v30
	v_med3_f32 v31, v34, s57, v196
	v_rcp_f32_e32 v30, v30
	v_fmamk_f32 v33, v163, 0x3c800000, v3
	v_mul_f32_e32 v24, v27, v24
	v_add_f32_e32 v27, 1.0, v31
	v_med3_f32 v33, v33, s57, v196
	v_mul_f32_e32 v27, v27, v24
	v_fmamk_f32 v24, v165, 0x3c800000, v5
	v_add_f32_e32 v33, 1.0, v33
	v_mul_f32_e32 v26, v26, v40
	v_med3_f32 v31, v24, s57, v196
	v_mov_b32_e32 v24, v181
	v_mul_f32_e32 v26, v33, v26
	v_mul_f32_e32 v30, v25, v30
	v_cvt_pk_fp8_f32 v24, v18, v19
	v_mov_b32_e32 v25, v181
	v_cvt_pk_fp8_f32 v25, v29, v26
	v_add_f32_e32 v18, 1.0, v31
	v_mul_f32_e32 v18, v18, v30
	v_cvt_pk_fp8_f32 v24, v23, v28 op_sel:[0,0,1]
	v_ashrrev_i32_e32 v23, 31, v22
	v_cvt_pk_fp8_f32 v25, v27, v18 op_sel:[0,0,1]
	v_lshlrev_b64 v[18:19], 11, v[22:23]
	v_fmamk_f32 v23, v158, 0x3c800000, v14
	v_min_f32_e32 v23, 0x40e00000, v23
	v_mul_f32_e32 v26, 0xbfd9db23, v23
	v_mul_f32_e32 v26, 0x3fb8aa3b, v26
	v_exp_f32_e32 v26, v26
	v_lshl_add_u64 v[18:19], s[8:9], 0, v[18:19]
	v_lshl_add_u64 v[18:19], v[18:19], 0, v[20:21]
	global_store_dwordx2 v[18:19], v[24:25], off
	v_add_f32_e32 v25, 1.0, v26
	v_fmamk_f32 v26, v159, 0x3c800000, v15
	v_min_f32_e32 v26, 0x40e00000, v26
	v_mul_f32_e32 v27, 0xbfd9db23, v26
	v_mul_f32_e32 v27, 0x3fb8aa3b, v27
	v_rcp_f32_e32 v25, v25
	v_exp_f32_e32 v27, v27
	v_fmamk_f32 v28, v161, 0x3c800000, v17
	v_min_f32_e32 v28, 0x40e00000, v28
	v_mul_f32_e32 v23, v23, v25
	v_add_f32_e32 v25, 1.0, v27
	v_rcp_f32_e32 v25, v25
	v_mul_f32_e32 v29, 0xbfd9db23, v28
	v_mul_f32_e32 v29, 0x3fb8aa3b, v29
	v_exp_f32_e32 v29, v29
	v_mul_f32_e32 v25, v26, v25
	v_fmamk_f32 v26, v160, 0x3c800000, v16
	v_min_f32_e32 v26, 0x40e00000, v26
	v_mul_f32_e32 v27, 0xbfd9db23, v26
	v_mul_f32_e32 v27, 0x3fb8aa3b, v27
	v_exp_f32_e32 v27, v27
	v_fmamk_f32 v30, v151, 0x3c800000, v7
	v_min_f32_e32 v30, 0x40e00000, v30
	v_mul_f32_e32 v31, 0xbfd9db23, v30
	v_add_f32_e32 v27, 1.0, v27
	v_rcp_f32_e32 v27, v27
	v_mul_f32_e32 v31, 0x3fb8aa3b, v31
	v_exp_f32_e32 v31, v31
	v_fmamk_f32 v24, v154, 0x3c800000, v10
	v_mul_f32_e32 v26, v26, v27
	v_add_f32_e32 v27, 1.0, v29
	v_rcp_f32_e32 v27, v27
	v_med3_f32 v24, v24, s57, v196
	v_add_f32_e32 v24, 1.0, v24
	v_mul_f32_e32 v23, v24, v23
	v_mul_f32_e32 v27, v28, v27
	v_fmamk_f32 v28, v150, 0x3c800000, v6
	v_min_f32_e32 v28, 0x40e00000, v28
	v_mul_f32_e32 v29, 0xbfd9db23, v28
	v_mul_f32_e32 v29, 0x3fb8aa3b, v29
	v_exp_f32_e32 v29, v29
	v_fmamk_f32 v24, v155, 0x3c800000, v11
	v_med3_f32 v24, v24, s57, v196
	v_add_f32_e32 v24, 1.0, v24
	v_add_f32_e32 v29, 1.0, v29
	v_rcp_f32_e32 v29, v29
	v_mul_f32_e32 v25, v24, v25
	v_fmamk_f32 v24, v156, 0x3c800000, v12
	v_med3_f32 v24, v24, s57, v196
	v_mul_f32_e32 v28, v28, v29
	v_add_f32_e32 v29, 1.0, v31
	v_rcp_f32_e32 v29, v29
	v_add_f32_e32 v24, 1.0, v24
	v_mul_f32_e32 v26, v24, v26
	v_fmamk_f32 v24, v157, 0x3c800000, v13
	v_mul_f32_e32 v29, v30, v29
	v_fmamk_f32 v30, v152, 0x3c800000, v8
	v_min_f32_e32 v30, 0x40e00000, v30
	v_mul_f32_e32 v31, 0xbfd9db23, v30
	v_med3_f32 v24, v24, s57, v196
	v_mul_f32_e32 v31, 0x3fb8aa3b, v31
	v_add_f32_e32 v24, 1.0, v24
; __device__ __forceinline__ unsigned pk4_fp8(float a, float b, float c, float d) { int p = __builtin_amdgcn_cvt_pk_fp8_f32(a, b, 0, false); p = __builtin_amdgcn_cvt_pk_fp8_f32(c, d, p, true); return (unsigned)p; }
;     __device__ __forceinline__ void operator()(const f32x4 (&acc)[2][2][4][2], const Unit& u, int wr, int wc, int fr, int fq) const {
;     ...
;         for (int ai = 0; ai < 2; ++ai)
; #pragma unroll
;             for (int m = 0; m < 4; ++m) { float r[8];
; #pragma unroll
;                 for (int n = 0; n < 2; ++n)
; #pragma unroll
;                     for (int j = 0; j < 4; ++j) {
;                         float g = acc[ai][0][m][n][j] * W8_INV + bg[n][j], uu = acc[ai][1][m][n][j] * W8_INV + bu[n][j];
;                         g = fminf(g, 7.0f); uu = fminf(fmaxf(uu, -7.0f), 7.0f);
;                         const float glu = g * __builtin_amdgcn_rcpf(1.0f + __expf(-1.702f * g));
;                         r[n * 4 + j] = (uu + 1.0f) * glu; }
;                 u32x2 w; w.x = pk4_fp8(r[0], r[1], r[2], r[3]); w.y = pk4_fp8(r[4], r[5], r[6], r[7]);
;                 *(u32x2*)(O + (size_t)(row0 + ai * HALF + m * 16) * DM + cc) = w; }
	v_exp_f32_e32 v31, v31
	v_mul_f32_e32 v27, v24, v27
	v_fmamk_f32 v24, v146, 0x3c800000, v2
	v_med3_f32 v24, v24, s57, v196
	v_fmamk_f32 v32, v153, 0x3c800000, v9
	v_add_f32_e32 v24, 1.0, v24
	v_min_f32_e32 v32, 0x40e00000, v32
	v_mul_f32_e32 v28, v24, v28
	v_fmamk_f32 v24, v147, 0x3c800000, v3
	v_add_f32_e32 v31, 1.0, v31
	v_mul_f32_e32 v33, 0xbfd9db23, v32
	v_med3_f32 v24, v24, s57, v196
	v_rcp_f32_e32 v31, v31
	v_mul_f32_e32 v33, 0x3fb8aa3b, v33
	v_add_f32_e32 v24, 1.0, v24
	v_exp_f32_e32 v33, v33
	v_mul_f32_e32 v29, v24, v29
	v_fmamk_f32 v24, v148, 0x3c800000, v4
	v_med3_f32 v24, v24, s57, v196
	v_mul_f32_e32 v30, v30, v31
	v_add_f32_e32 v24, 1.0, v24
	v_add_f32_e32 v31, 1.0, v33
	v_mul_f32_e32 v30, v24, v30
	v_fmamk_f32 v24, v149, 0x3c800000, v5
	v_rcp_f32_e32 v31, v31
	v_med3_f32 v33, v24, s57, v196
	v_mov_b32_e32 v24, v181
	v_cvt_pk_fp8_f32 v24, v23, v25
	v_mov_b32_e32 v25, v181
	v_cvt_pk_fp8_f32 v25, v28, v29
	v_mul_f32_e32 v31, v32, v31
	v_add_f32_e32 v23, 1.0, v33
	v_mul_f32_e32 v23, v23, v31
	v_cvt_pk_fp8_f32 v24, v26, v27 op_sel:[0,0,1]
	v_cvt_pk_fp8_f32 v25, v30, v23 op_sel:[0,0,1]
	v_or_b32_e32 v26, 16, v22
	v_fmamk_f32 v23, v142, 0x3c800000, v14
	v_ashrrev_i32_e32 v27, 31, v26
	v_min_f32_e32 v23, 0x40e00000, v23
	v_lshlrev_b64 v[26:27], 11, v[26:27]
	v_mul_f32_e32 v28, 0xbfd9db23, v23
	v_lshl_add_u64 v[26:27], s[8:9], 0, v[26:27]
	v_mul_f32_e32 v28, 0x3fb8aa3b, v28
	v_exp_f32_e32 v28, v28
	v_lshl_add_u64 v[26:27], v[26:27], 0, v[20:21]
	global_store_dwordx2 v[26:27], v[24:25], off
	v_fmamk_f32 v26, v143, 0x3c800000, v15
	v_min_f32_e32 v26, 0x40e00000, v26
	v_mul_f32_e32 v27, 0xbfd9db23, v26
	v_add_f32_e32 v25, 1.0, v28
	v_mul_f32_e32 v27, 0x3fb8aa3b, v27
	v_rcp_f32_e32 v25, v25
	v_exp_f32_e32 v27, v27
	v_fmamk_f32 v28, v145, 0x3c800000, v17
	v_min_f32_e32 v28, 0x40e00000, v28
	v_mul_f32_e32 v23, v23, v25
	v_add_f32_e32 v25, 1.0, v27
	v_rcp_f32_e32 v25, v25
	v_mul_f32_e32 v29, 0xbfd9db23, v28
	v_mul_f32_e32 v29, 0x3fb8aa3b, v29
	v_exp_f32_e32 v29, v29
	v_mul_f32_e32 v25, v26, v25
	v_fmamk_f32 v26, v144, 0x3c800000, v16
	v_min_f32_e32 v26, 0x40e00000, v26
	v_mul_f32_e32 v27, 0xbfd9db23, v26
	v_mul_f32_e32 v27, 0x3fb8aa3b, v27
	v_exp_f32_e32 v27, v27
	v_fmamk_f32 v30, v135, 0x3c800000, v7
	v_min_f32_e32 v30, 0x40e00000, v30
	v_mul_f32_e32 v31, 0xbfd9db23, v30
	v_add_f32_e32 v27, 1.0, v27
	v_rcp_f32_e32 v27, v27
	v_mul_f32_e32 v31, 0x3fb8aa3b, v31
	v_exp_f32_e32 v31, v31
	v_fmamk_f32 v24, v138, 0x3c800000, v10
	v_mul_f32_e32 v26, v26, v27
	v_add_f32_e32 v27, 1.0, v29
	v_rcp_f32_e32 v27, v27
	v_med3_f32 v24, v24, s57, v196
	v_add_f32_e32 v24, 1.0, v24
	v_mul_f32_e32 v23, v24, v23
	v_mul_f32_e32 v27, v28, v27
	v_fmamk_f32 v28, v134, 0x3c800000, v6
	v_min_f32_e32 v28, 0x40e00000, v28
	v_mul_f32_e32 v29, 0xbfd9db23, v28
	v_mul_f32_e32 v29, 0x3fb8aa3b, v29
	v_exp_f32_e32 v29, v29
	v_fmamk_f32 v24, v139, 0x3c800000, v11
	v_med3_f32 v24, v24, s57, v196
	v_add_f32_e32 v24, 1.0, v24
	v_add_f32_e32 v29, 1.0, v29
	v_rcp_f32_e32 v29, v29
	v_mul_f32_e32 v25, v24, v25
	v_fmamk_f32 v24, v140, 0x3c800000, v12
	v_med3_f32 v24, v24, s57, v196
	v_mul_f32_e32 v28, v28, v29
	v_add_f32_e32 v29, 1.0, v31
	v_rcp_f32_e32 v29, v29
	v_add_f32_e32 v24, 1.0, v24
	v_mul_f32_e32 v26, v24, v26
	v_fmamk_f32 v24, v141, 0x3c800000, v13
	v_mul_f32_e32 v29, v30, v29
	v_fmamk_f32 v30, v136, 0x3c800000, v8
	v_min_f32_e32 v30, 0x40e00000, v30
	v_mul_f32_e32 v31, 0xbfd9db23, v30
	v_med3_f32 v24, v24, s57, v196
	v_mul_f32_e32 v31, 0x3fb8aa3b, v31
	v_add_f32_e32 v24, 1.0, v24
	v_exp_f32_e32 v31, v31
	v_mul_f32_e32 v27, v24, v27
	v_fmamk_f32 v24, v130, 0x3c800000, v2
	v_med3_f32 v24, v24, s57, v196
	v_fmamk_f32 v32, v137, 0x3c800000, v9
	v_add_f32_e32 v24, 1.0, v24
	v_min_f32_e32 v32, 0x40e00000, v32
	v_mul_f32_e32 v28, v24, v28
	v_fmamk_f32 v24, v131, 0x3c800000, v3
	v_add_f32_e32 v31, 1.0, v31
	v_mul_f32_e32 v33, 0xbfd9db23, v32
	v_med3_f32 v24, v24, s57, v196
	v_rcp_f32_e32 v31, v31
	v_mul_f32_e32 v33, 0x3fb8aa3b, v33
	v_add_f32_e32 v24, 1.0, v24
	v_exp_f32_e32 v33, v33
	v_mul_f32_e32 v29, v24, v29
	v_fmamk_f32 v24, v132, 0x3c800000, v4
	v_med3_f32 v24, v24, s57, v196
	v_mul_f32_e32 v30, v30, v31
	v_add_f32_e32 v24, 1.0, v24
	v_add_f32_e32 v31, 1.0, v33
	v_mul_f32_e32 v30, v24, v30
	v_fmamk_f32 v24, v133, 0x3c800000, v5
	v_rcp_f32_e32 v31, v31
	v_med3_f32 v33, v24, s57, v196
	v_mov_b32_e32 v24, v181
	v_cvt_pk_fp8_f32 v24, v23, v25
	v_mov_b32_e32 v25, v181
	v_cvt_pk_fp8_f32 v25, v28, v29
	v_mul_f32_e32 v31, v32, v31
	v_add_f32_e32 v23, 1.0, v33
	v_mul_f32_e32 v23, v23, v31
	v_cvt_pk_fp8_f32 v24, v26, v27 op_sel:[0,0,1]
	v_cvt_pk_fp8_f32 v25, v30, v23 op_sel:[0,0,1]
	v_or_b32_e32 v26, 32, v22
	v_fmamk_f32 v23, v126, 0x3c800000, v14
	v_ashrrev_i32_e32 v27, 31, v26
	v_min_f32_e32 v23, 0x40e00000, v23
	v_lshlrev_b64 v[26:27], 11, v[26:27]
	v_mul_f32_e32 v28, 0xbfd9db23, v23
	v_lshl_add_u64 v[26:27], s[8:9], 0, v[26:27]
	v_mul_f32_e32 v28, 0x3fb8aa3b, v28
	v_exp_f32_e32 v28, v28
	v_lshl_add_u64 v[26:27], v[26:27], 0, v[20:21]
	global_store_dwordx2 v[26:27], v[24:25], off
	v_fmamk_f32 v26, v127, 0x3c800000, v15
	v_min_f32_e32 v26, 0x40e00000, v26
	v_mul_f32_e32 v27, 0xbfd9db23, v26
	v_add_f32_e32 v25, 1.0, v28
	v_mul_f32_e32 v27, 0x3fb8aa3b, v27
	v_rcp_f32_e32 v25, v25
	v_exp_f32_e32 v27, v27
	v_fmamk_f32 v28, v129, 0x3c800000, v17
	v_min_f32_e32 v28, 0x40e00000, v28
	v_mul_f32_e32 v23, v23, v25
	v_add_f32_e32 v25, 1.0, v27
	v_rcp_f32_e32 v25, v25
	v_mul_f32_e32 v29, 0xbfd9db23, v28
	v_mul_f32_e32 v29, 0x3fb8aa3b, v29
	v_exp_f32_e32 v29, v29
	v_mul_f32_e32 v25, v26, v25
	v_fmamk_f32 v26, v128, 0x3c800000, v16
	v_min_f32_e32 v26, 0x40e00000, v26
	v_mul_f32_e32 v27, 0xbfd9db23, v26
; __device__ __forceinline__ unsigned pk4_fp8(float a, float b, float c, float d) { int p = __builtin_amdgcn_cvt_pk_fp8_f32(a, b, 0, false); p = __builtin_amdgcn_cvt_pk_fp8_f32(c, d, p, true); return (unsigned)p; }
;     __device__ __forceinline__ void operator()(const f32x4 (&acc)[2][2][4][2], const Unit& u, int wr, int wc, int fr, int fq) const {
;     ...
;         for (int ai = 0; ai < 2; ++ai)
; #pragma unroll
;             for (int m = 0; m < 4; ++m) { float r[8];
; #pragma unroll
;                 for (int n = 0; n < 2; ++n)
; #pragma unroll
;                     for (int j = 0; j < 4; ++j) {
;                         float g = acc[ai][0][m][n][j] * W8_INV + bg[n][j], uu = acc[ai][1][m][n][j] * W8_INV + bu[n][j];
;                         g = fminf(g, 7.0f); uu = fminf(fmaxf(uu, -7.0f), 7.0f);
;                         const float glu = g * __builtin_amdgcn_rcpf(1.0f + __expf(-1.702f * g));
;                         r[n * 4 + j] = (uu + 1.0f) * glu; }
;                 u32x2 w; w.x = pk4_fp8(r[0], r[1], r[2], r[3]); w.y = pk4_fp8(r[4], r[5], r[6], r[7]);
;                 *(u32x2*)(O + (size_t)(row0 + ai * HALF + m * 16) * DM + cc) = w; }
	v_mul_f32_e32 v27, 0x3fb8aa3b, v27
	v_exp_f32_e32 v27, v27
	v_fmamk_f32 v30, v119, 0x3c800000, v7
	v_min_f32_e32 v30, 0x40e00000, v30
	v_mul_f32_e32 v31, 0xbfd9db23, v30
	v_add_f32_e32 v27, 1.0, v27
	v_rcp_f32_e32 v27, v27
	v_mul_f32_e32 v31, 0x3fb8aa3b, v31
	v_exp_f32_e32 v31, v31
	v_fmamk_f32 v24, v122, 0x3c800000, v10
	v_mul_f32_e32 v26, v26, v27
	v_add_f32_e32 v27, 1.0, v29
	v_rcp_f32_e32 v27, v27
	v_med3_f32 v24, v24, s57, v196
	v_add_f32_e32 v24, 1.0, v24
	v_mul_f32_e32 v23, v24, v23
	v_mul_f32_e32 v27, v28, v27
	v_fmamk_f32 v28, v118, 0x3c800000, v6
	v_min_f32_e32 v28, 0x40e00000, v28
	v_mul_f32_e32 v29, 0xbfd9db23, v28
	v_mul_f32_e32 v29, 0x3fb8aa3b, v29
	v_exp_f32_e32 v29, v29
	v_fmamk_f32 v24, v123, 0x3c800000, v11
	v_med3_f32 v24, v24, s57, v196
	v_add_f32_e32 v24, 1.0, v24
	v_add_f32_e32 v29, 1.0, v29
	v_rcp_f32_e32 v29, v29
	v_mul_f32_e32 v25, v24, v25
	v_fmamk_f32 v24, v124, 0x3c800000, v12
	v_med3_f32 v24, v24, s57, v196
	v_mul_f32_e32 v28, v28, v29
	v_add_f32_e32 v29, 1.0, v31
	v_rcp_f32_e32 v29, v29
	v_add_f32_e32 v24, 1.0, v24
	v_mul_f32_e32 v26, v24, v26
	v_fmamk_f32 v24, v125, 0x3c800000, v13
	v_mul_f32_e32 v29, v30, v29
	v_fmamk_f32 v30, v120, 0x3c800000, v8
	v_min_f32_e32 v30, 0x40e00000, v30
	v_mul_f32_e32 v31, 0xbfd9db23, v30
	v_med3_f32 v24, v24, s57, v196
	v_mul_f32_e32 v31, 0x3fb8aa3b, v31
	v_add_f32_e32 v24, 1.0, v24
	v_exp_f32_e32 v31, v31
	v_mul_f32_e32 v27, v24, v27
	v_fmamk_f32 v24, v114, 0x3c800000, v2
	v_med3_f32 v24, v24, s57, v196
	v_fmamk_f32 v32, v121, 0x3c800000, v9
	v_add_f32_e32 v24, 1.0, v24
	v_min_f32_e32 v32, 0x40e00000, v32
	v_mul_f32_e32 v28, v24, v28
	v_fmamk_f32 v24, v115, 0x3c800000, v3
	v_add_f32_e32 v31, 1.0, v31
	v_mul_f32_e32 v33, 0xbfd9db23, v32
	v_med3_f32 v24, v24, s57, v196
	v_rcp_f32_e32 v31, v31
	v_mul_f32_e32 v33, 0x3fb8aa3b, v33
	v_add_f32_e32 v24, 1.0, v24
	v_exp_f32_e32 v33, v33
	v_mul_f32_e32 v29, v24, v29
	v_fmamk_f32 v24, v116, 0x3c800000, v4
	v_med3_f32 v24, v24, s57, v196
	v_mul_f32_e32 v30, v30, v31
	v_add_f32_e32 v24, 1.0, v24
	v_add_f32_e32 v31, 1.0, v33
	v_mul_f32_e32 v30, v24, v30
	v_fmamk_f32 v24, v117, 0x3c800000, v5
	v_rcp_f32_e32 v31, v31
	v_med3_f32 v33, v24, s57, v196
	v_mov_b32_e32 v24, v181
	v_cvt_pk_fp8_f32 v24, v23, v25
	v_mov_b32_e32 v25, v181
	v_cvt_pk_fp8_f32 v25, v28, v29
	v_mul_f32_e32 v31, v32, v31
	v_add_f32_e32 v23, 1.0, v33
	v_mul_f32_e32 v23, v23, v31
	v_or_b32_e32 v22, 48, v22
	v_cvt_pk_fp8_f32 v25, v30, v23 op_sel:[0,0,1]
	v_ashrrev_i32_e32 v23, 31, v22
	v_lshlrev_b64 v[22:23], 11, v[22:23]
	v_lshl_add_u64 v[22:23], s[8:9], 0, v[22:23]
	v_lshl_add_u64 v[20:21], v[22:23], 0, v[20:21]
	v_fmamk_f32 v22, v111, 0x3c800000, v15
	v_min_f32_e32 v22, 0x40e00000, v22
	v_mul_f32_e32 v23, 0xbfd9db23, v22
	v_mul_f32_e32 v23, 0x3fb8aa3b, v23
	v_exp_f32_e32 v23, v23
	v_cvt_pk_fp8_f32 v24, v26, v27 op_sel:[0,0,1]
	v_fmamk_f32 v26, v110, 0x3c800000, v14
	v_min_f32_e32 v26, 0x40e00000, v26
	v_add_f32_e32 v23, 1.0, v23
	v_mul_f32_e32 v27, 0xbfd9db23, v26
	v_rcp_f32_e32 v23, v23
	v_mul_f32_e32 v27, 0x3fb8aa3b, v27
	v_exp_f32_e32 v27, v27
	global_store_dwordx2 v[20:21], v[24:25], off
	v_mul_f32_e32 v22, v22, v23
	v_fmamk_f32 v23, v112, 0x3c800000, v16
	v_min_f32_e32 v23, 0x40e00000, v23
	v_add_f32_e32 v21, 1.0, v27
	v_mul_f32_e32 v24, 0xbfd9db23, v23
	v_rcp_f32_e32 v21, v21
	v_mul_f32_e32 v24, 0x3fb8aa3b, v24
	v_exp_f32_e32 v24, v24
	v_fmamk_f32 v25, v113, 0x3c800000, v17
	v_min_f32_e32 v25, 0x40e00000, v25
	v_mul_f32_e32 v21, v26, v21
	v_mul_f32_e32 v26, 0xbfd9db23, v25
	v_add_f32_e32 v24, 1.0, v24
	v_mul_f32_e32 v26, 0x3fb8aa3b, v26
	v_rcp_f32_e32 v24, v24
	v_exp_f32_e32 v26, v26
	v_fmamk_f32 v27, v103, 0x3c800000, v7
	v_min_f32_e32 v27, 0x40e00000, v27
	v_mul_f32_e32 v23, v23, v24
	v_add_f32_e32 v24, 1.0, v26
	v_rcp_f32_e32 v24, v24
	v_mul_f32_e32 v28, 0xbfd9db23, v27
	v_mul_f32_e32 v28, 0x3fb8aa3b, v28
	v_exp_f32_e32 v28, v28
	v_mul_f32_e32 v24, v25, v24
	v_fmamk_f32 v25, v102, 0x3c800000, v6
	v_min_f32_e32 v25, 0x40e00000, v25
	v_mul_f32_e32 v26, 0xbfd9db23, v25
	v_mul_f32_e32 v26, 0x3fb8aa3b, v26
	v_exp_f32_e32 v26, v26
	v_fmamk_f32 v20, v106, 0x3c800000, v10
	v_med3_f32 v20, v20, s57, v196
	v_add_f32_e32 v20, 1.0, v20
	v_add_f32_e32 v26, 1.0, v26
	v_rcp_f32_e32 v26, v26
	v_mul_f32_e32 v21, v20, v21
	v_fmamk_f32 v20, v107, 0x3c800000, v11
	v_med3_f32 v20, v20, s57, v196
	v_mul_f32_e32 v25, v25, v26
	v_add_f32_e32 v26, 1.0, v28
	v_rcp_f32_e32 v26, v26
	v_add_f32_e32 v20, 1.0, v20
	v_mul_f32_e32 v22, v20, v22
	v_fmamk_f32 v20, v108, 0x3c800000, v12
	v_med3_f32 v20, v20, s57, v196
	v_mul_f32_e32 v26, v27, v26
	v_fmamk_f32 v27, v104, 0x3c800000, v8
	v_add_f32_e32 v20, 1.0, v20
	v_min_f32_e32 v27, 0x40e00000, v27
	v_mul_f32_e32 v23, v20, v23
	v_fmamk_f32 v20, v109, 0x3c800000, v13
	v_mul_f32_e32 v28, 0xbfd9db23, v27
	v_med3_f32 v20, v20, s57, v196
	v_mul_f32_e32 v28, 0x3fb8aa3b, v28
	v_add_f32_e32 v20, 1.0, v20
	v_exp_f32_e32 v28, v28
	v_mul_f32_e32 v24, v20, v24
	v_fmamk_f32 v20, v98, 0x3c800000, v2
	v_med3_f32 v20, v20, s57, v196
	v_fmamk_f32 v29, v105, 0x3c800000, v9
	v_add_f32_e32 v20, 1.0, v20
	v_min_f32_e32 v29, 0x40e00000, v29
	v_mul_f32_e32 v25, v20, v25
	v_fmamk_f32 v20, v99, 0x3c800000, v3
	v_add_f32_e32 v28, 1.0, v28
	v_mul_f32_e32 v30, 0xbfd9db23, v29
	v_med3_f32 v20, v20, s57, v196
	v_rcp_f32_e32 v28, v28
	v_mul_f32_e32 v30, 0x3fb8aa3b, v30
	v_add_f32_e32 v20, 1.0, v20
	v_exp_f32_e32 v30, v30
	v_mul_f32_e32 v26, v20, v26
	v_fmamk_f32 v20, v100, 0x3c800000, v4
	v_med3_f32 v20, v20, s57, v196
	v_mul_f32_e32 v27, v27, v28
	v_add_f32_e32 v20, 1.0, v20
	v_add_f32_e32 v28, 1.0, v30
	v_mul_f32_e32 v27, v20, v27
	v_fmamk_f32 v20, v101, 0x3c800000, v5
; __device__ __forceinline__ unsigned pk4_fp8(float a, float b, float c, float d) { int p = __builtin_amdgcn_cvt_pk_fp8_f32(a, b, 0, false); p = __builtin_amdgcn_cvt_pk_fp8_f32(c, d, p, true); return (unsigned)p; }
; __device__ __forceinline__ unsigned pk4_fp8_scaled(float a, float b, float c, float d) { s16x2 r = {0, 0}; r = __builtin_amdgcn_cvt_scalef32_pk_fp8_f32(r, a, b, pg8::W8_INV, false); r = __builtin_amdgcn_cvt_scalef32_pk_fp8_f32(r, c, d, pg8::W8_INV, true); return __builtin_bit_cast(unsigned, r); }
;     __device__ __forceinline__ void operator()(const f32x4 (&acc)[2][2][4][2], const Unit& u, int wr, int wc, int fr, int fq) const {
;     ...
;         for (int ai = 0; ai < 2; ++ai)
; #pragma unroll
;             for (int m = 0; m < 4; ++m) { float r[8];
; #pragma unroll
;                 for (int n = 0; n < 2; ++n)
; #pragma unroll
;                     for (int j = 0; j < 4; ++j) {
;                         float g = acc[ai][0][m][n][j] * W8_INV + bg[n][j], uu = acc[ai][1][m][n][j] * W8_INV + bu[n][j];
;                         g = fminf(g, 7.0f); uu = fminf(fmaxf(uu, -7.0f), 7.0f);
;                         const float glu = g * __builtin_amdgcn_rcpf(1.0f + __expf(-1.702f * g));
;                         r[n * 4 + j] = (uu + 1.0f) * glu; }
;                 u32x2 w; w.x = pk4_fp8(r[0], r[1], r[2], r[3]); w.y = pk4_fp8(r[4], r[5], r[6], r[7]);
;                 *(u32x2*)(O + (size_t)(row0 + ai * HALF + m * 16) * DM + cc) = w; }
; __device__ __forceinline__ void sjob_load(const SJob& c, f32x4 (&v)[8]) {
; #pragma unroll
;     for (int r = 0; r < 8; ++r) v[r] = __builtin_nontemporal_load((const f32x4*)(c.src + (size_t)r * c.ld));
; }
; __device__ __forceinline__ void sjob_store(const SJob& c, const f32x4 (&v)[8]) {
; #pragma unroll
;     for (int jn = 0; jn < 4; ++jn) { u32x2 o;
;         o.x = pk4_fp8_scaled(v[0][jn], v[1][jn], v[2][jn], v[3][jn]); o.y = pk4_fp8_scaled(v[4][jn], v[5][jn], v[6][jn], v[7][jn]);
;         __builtin_nontemporal_store(o, (u32x2*)(c.dst + (size_t)jn * 2048)); }
; }
	v_rcp_f32_e32 v28, v28
	v_med3_f32 v30, v20, s57, v196
	v_mov_b32_e32 v20, v181
	v_cvt_pk_fp8_f32 v20, v21, v22
	v_mov_b32_e32 v21, v181
	v_cvt_pk_fp8_f32 v21, v25, v26
	v_mul_f32_e32 v28, v29, v28
	v_add_f32_e32 v22, 1.0, v30
	v_mul_f32_e32 v22, v22, v28
	v_cvt_pk_fp8_f32 v21, v27, v22 op_sel:[0,0,1]
	v_fmamk_f32 v22, v94, 0x3c800000, v14
	v_cvt_pk_fp8_f32 v20, v23, v24 op_sel:[0,0,1]
	v_min_f32_e32 v24, 0x40e00000, v22
	v_mul_f32_e32 v22, 0xbfd9db23, v24
	v_mul_f32_e32 v22, 0x3fb8aa3b, v22
	v_exp_f32_e32 v25, v22
	v_add_co_u32_e32 v22, vcc, s58, v18
	v_fmamk_f32 v27, v87, 0x3c800000, v7
	s_nop 0
	v_addc_co_u32_e32 v23, vcc, 0, v19, vcc
	global_store_dwordx2 v[22:23], v[20:21], off
	v_fmamk_f32 v22, v95, 0x3c800000, v15
	v_min_f32_e32 v22, 0x40e00000, v22
	v_mul_f32_e32 v23, 0xbfd9db23, v22
	v_mul_f32_e32 v23, 0x3fb8aa3b, v23
	v_exp_f32_e32 v23, v23
	v_add_f32_e32 v21, 1.0, v25
	v_rcp_f32_e32 v21, v21
	v_fmamk_f32 v25, v97, 0x3c800000, v17
	v_add_f32_e32 v23, 1.0, v23
	v_rcp_f32_e32 v23, v23
	v_mul_f32_e32 v21, v24, v21
	v_min_f32_e32 v25, 0x40e00000, v25
	v_mul_f32_e32 v26, 0xbfd9db23, v25
	v_mul_f32_e32 v22, v22, v23
	v_fmamk_f32 v23, v96, 0x3c800000, v16
	v_min_f32_e32 v23, 0x40e00000, v23
	v_mul_f32_e32 v24, 0xbfd9db23, v23
	v_mul_f32_e32 v24, 0x3fb8aa3b, v24
	v_exp_f32_e32 v24, v24
	v_mul_f32_e32 v26, 0x3fb8aa3b, v26
	v_exp_f32_e32 v26, v26
	v_min_f32_e32 v27, 0x40e00000, v27
	v_add_f32_e32 v24, 1.0, v24
	v_rcp_f32_e32 v24, v24
	v_mul_f32_e32 v28, 0xbfd9db23, v27
	v_mul_f32_e32 v28, 0x3fb8aa3b, v28
	v_exp_f32_e32 v28, v28
	v_mul_f32_e32 v23, v23, v24
	v_add_f32_e32 v24, 1.0, v26
	v_rcp_f32_e32 v24, v24
	v_fmamk_f32 v20, v90, 0x3c800000, v10
	v_med3_f32 v20, v20, s57, v196
	v_add_f32_e32 v20, 1.0, v20
	v_mul_f32_e32 v24, v25, v24
	v_fmamk_f32 v25, v86, 0x3c800000, v6
	v_min_f32_e32 v25, 0x40e00000, v25
	v_mul_f32_e32 v26, 0xbfd9db23, v25
	v_mul_f32_e32 v26, 0x3fb8aa3b, v26
	v_exp_f32_e32 v26, v26
	v_mul_f32_e32 v21, v20, v21
	v_fmamk_f32 v20, v91, 0x3c800000, v11
	v_med3_f32 v20, v20, s57, v196
	v_add_f32_e32 v26, 1.0, v26
	v_rcp_f32_e32 v26, v26
	v_add_f32_e32 v20, 1.0, v20
	v_mul_f32_e32 v22, v20, v22
	v_fmamk_f32 v20, v92, 0x3c800000, v12
	v_mul_f32_e32 v25, v25, v26
	v_add_f32_e32 v26, 1.0, v28
	v_rcp_f32_e32 v26, v26
	v_med3_f32 v20, v20, s57, v196
	v_add_f32_e32 v20, 1.0, v20
	v_mul_f32_e32 v23, v20, v23
	v_mul_f32_e32 v26, v27, v26
	v_fmamk_f32 v27, v88, 0x3c800000, v8
	v_min_f32_e32 v27, 0x40e00000, v27
	v_fmamk_f32 v20, v93, 0x3c800000, v13
	v_mul_f32_e32 v28, 0xbfd9db23, v27
	v_med3_f32 v20, v20, s57, v196
	v_mul_f32_e32 v28, 0x3fb8aa3b, v28
	v_add_f32_e32 v20, 1.0, v20
	v_exp_f32_e32 v28, v28
	v_mul_f32_e32 v24, v20, v24
	v_fmamk_f32 v20, v82, 0x3c800000, v2
	v_med3_f32 v20, v20, s57, v196
	v_fmamk_f32 v29, v89, 0x3c800000, v9
	v_add_f32_e32 v20, 1.0, v20
	v_min_f32_e32 v29, 0x40e00000, v29
	v_mul_f32_e32 v25, v20, v25
	v_fmamk_f32 v20, v83, 0x3c800000, v3
	v_add_f32_e32 v28, 1.0, v28
	v_mul_f32_e32 v30, 0xbfd9db23, v29
	v_med3_f32 v20, v20, s57, v196
	v_rcp_f32_e32 v28, v28
	v_mul_f32_e32 v30, 0x3fb8aa3b, v30
	v_add_f32_e32 v20, 1.0, v20
	v_exp_f32_e32 v30, v30
	v_mul_f32_e32 v26, v20, v26
	v_fmamk_f32 v20, v84, 0x3c800000, v4
	v_med3_f32 v20, v20, s57, v196
	v_mul_f32_e32 v27, v27, v28
	v_add_f32_e32 v20, 1.0, v20
	v_add_f32_e32 v28, 1.0, v30
	v_mul_f32_e32 v27, v20, v27
	v_fmamk_f32 v20, v85, 0x3c800000, v5
	v_rcp_f32_e32 v28, v28
	v_med3_f32 v30, v20, s57, v196
	v_mov_b32_e32 v20, v181
	v_cvt_pk_fp8_f32 v20, v21, v22
	v_mov_b32_e32 v21, v181
	v_cvt_pk_fp8_f32 v21, v25, v26
	v_mul_f32_e32 v28, v29, v28
	v_add_f32_e32 v22, 1.0, v30
	v_mul_f32_e32 v22, v22, v28
	v_cvt_pk_fp8_f32 v21, v27, v22 op_sel:[0,0,1]
	v_fmamk_f32 v22, v78, 0x3c800000, v14
	v_cvt_pk_fp8_f32 v20, v23, v24 op_sel:[0,0,1]
	v_min_f32_e32 v24, 0x40e00000, v22
	v_mul_f32_e32 v22, 0xbfd9db23, v24
	v_mul_f32_e32 v22, 0x3fb8aa3b, v22
	v_exp_f32_e32 v25, v22
	v_add_co_u32_e32 v22, vcc, s59, v18
	v_fmamk_f32 v27, v71, 0x3c800000, v7
	s_nop 0
	v_addc_co_u32_e32 v23, vcc, 0, v19, vcc
	global_store_dwordx2 v[22:23], v[20:21], off
	s_cmp_lg_u32 s82, 0
	s_cbranch_scc0 .Le2_skip
	s_waitcnt vmcnt(6)
	v_cvt_scalef32_pk_fp8_f32 v250, v218, v222, v254
	v_cvt_scalef32_pk_fp8_f32 v251, v234, v238, v254
	v_cvt_scalef32_pk_fp8_f32 v250, v226, v230, v254 op_sel:[0,0,0,1]
	v_cvt_scalef32_pk_fp8_f32 v251, v242, v246, v254 op_sel:[0,0,0,1]
	global_store_dwordx2 v253, v[250:251], s[90:91] nt
	v_cvt_scalef32_pk_fp8_f32 v250, v219, v223, v254
	v_cvt_scalef32_pk_fp8_f32 v251, v235, v239, v254
	v_cvt_scalef32_pk_fp8_f32 v250, v227, v231, v254 op_sel:[0,0,0,1]
	v_cvt_scalef32_pk_fp8_f32 v251, v243, v247, v254 op_sel:[0,0,0,1]
	global_store_dwordx2 v253, v[250:251], s[90:91] offset:2048 nt
	v_cvt_scalef32_pk_fp8_f32 v250, v220, v224, v254
	v_cvt_scalef32_pk_fp8_f32 v251, v236, v240, v254
	v_cvt_scalef32_pk_fp8_f32 v250, v228, v232, v254 op_sel:[0,0,0,1]
	v_cvt_scalef32_pk_fp8_f32 v251, v244, v248, v254 op_sel:[0,0,0,1]
	s_add_u32 s90, s90, 0x1000
	s_addc_u32 s91, s91, 0
	global_store_dwordx2 v253, v[250:251], s[90:91] nt
	v_cvt_scalef32_pk_fp8_f32 v250, v221, v225, v254
	v_cvt_scalef32_pk_fp8_f32 v251, v237, v241, v254
	v_cvt_scalef32_pk_fp8_f32 v250, v229, v233, v254 op_sel:[0,0,0,1]
	v_cvt_scalef32_pk_fp8_f32 v251, v245, v249, v254 op_sel:[0,0,0,1]
	global_store_dwordx2 v253, v[250:251], s[90:91] offset:2048 nt
	s_add_i32 s98, s98, 1
	s_lshr_b32 s90, s98, 1
	s_mul_i32 s90, s90, s83
	s_add_i32 s90, s90, s84
	s_cmp_lt_u32 s90, 0x8000
	s_cbranch_scc0 .Le2_no
	s_lshr_b32 s91, s90, 10
	s_lshl_b32 s91, s91, 11
	s_and_b32 s99, s90, 0x3c0
	s_lshl_b32 s99, s99, 1
	s_or_b32 s91, s91, s99
	s_and_b32 s99, s98, 1
	s_lshl_b32 s99, s99, 6
	s_or_b32 s91, s91, s99
	s_and_b32 s90, s90, 63
	s_or_b32 s90, s90, s91
	s_lshr_b32 s91, s90, 11
	s_and_b32 s99, s90, 0x7c0
	s_and_b32 s82, s90, 63
	s_lshl_b32 s32, s91, 24
	s_lshl_b32 s100, s99, 13
	s_add_i32 s32, s32, s100
	s_lshl_b32 s100, s82, 7
	s_add_i32 s32, s32, s100
	s_add_u32 s100, s86, s32
	s_addc_u32 s101, s87, 0
	s_lshl_b32 s32, s91, 22
	s_lshl_b32 s82, s82, 16
	s_add_i32 s32, s32, s82
	s_add_i32 s32, s32, s99
	s_add_u32 s90, s88, s32
	s_addc_u32 s91, s89, 0
	global_load_dwordx4 v[218:221], v252, s[100:101] nt
	s_add_u32 s100, s100, 0x2000
	s_addc_u32 s101, s101, 0
	global_load_dwordx4 v[222:225], v252, s[100:101] nt
	s_add_u32 s100, s100, 0x2000
	s_addc_u32 s101, s101, 0
	global_load_dwordx4 v[226:229], v252, s[100:101] nt
	s_add_u32 s100, s100, 0x2000
	s_addc_u32 s101, s101, 0
	global_load_dwordx4 v[230:233], v252, s[100:101] nt
	s_add_u32 s100, s100, 0x2000
	s_addc_u32 s101, s101, 0
	global_load_dwordx4 v[234:237], v252, s[100:101] nt
	s_add_u32 s100, s100, 0x2000
	s_addc_u32 s101, s101, 0
	global_load_dwordx4 v[238:241], v252, s[100:101] nt
	s_add_u32 s100, s100, 0x2000
	s_addc_u32 s101, s101, 0
	global_load_dwordx4 v[242:245], v252, s[100:101] nt
	s_add_u32 s100, s100, 0x2000
	s_addc_u32 s101, s101, 0
	global_load_dwordx4 v[246:249], v252, s[100:101] nt
	s_mov_b32 s82, 2
	s_branch .Le2_skip

; __device__ __forceinline__ unsigned pk4_fp8(float a, float b, float c, float d) { int p = __builtin_amdgcn_cvt_pk_fp8_f32(a, b, 0, false); p = __builtin_amdgcn_cvt_pk_fp8_f32(c, d, p, true); return (unsigned)p; }
;     __device__ __forceinline__ void operator()(const f32x4 (&acc)[2][2][4][2], const Unit& u, int wr, int wc, int fr, int fq) const {
;     ...
;         for (int ai = 0; ai < 2; ++ai)
; #pragma unroll
;             for (int m = 0; m < 4; ++m) { float r[8];
; #pragma unroll
;                 for (int n = 0; n < 2; ++n)
; #pragma unroll
;                     for (int j = 0; j < 4; ++j) {
;                         float g = acc[ai][0][m][n][j] * W8_INV + bg[n][j], uu = acc[ai][1][m][n][j] * W8_INV + bu[n][j];
;                         g = fminf(g, 7.0f); uu = fminf(fmaxf(uu, -7.0f), 7.0f);
;                         const float glu = g * __builtin_amdgcn_rcpf(1.0f + __expf(-1.702f * g));
;                         r[n * 4 + j] = (uu + 1.0f) * glu; }
;                 u32x2 w; w.x = pk4_fp8(r[0], r[1], r[2], r[3]); w.y = pk4_fp8(r[4], r[5], r[6], r[7]);
;                 *(u32x2*)(O + (size_t)(row0 + ai * HALF + m * 16) * DM + cc) = w; }
.Le2_skip:
	v_fmamk_f32 v22, v79, 0x3c800000, v15
	v_min_f32_e32 v22, 0x40e00000, v22
	v_mul_f32_e32 v23, 0xbfd9db23, v22
	v_mul_f32_e32 v23, 0x3fb8aa3b, v23
	v_exp_f32_e32 v23, v23
	v_add_f32_e32 v21, 1.0, v25
	v_rcp_f32_e32 v21, v21
	v_fmamk_f32 v25, v81, 0x3c800000, v17
	v_add_f32_e32 v23, 1.0, v23
	v_rcp_f32_e32 v23, v23
	v_mul_f32_e32 v21, v24, v21
	v_min_f32_e32 v25, 0x40e00000, v25
	v_mul_f32_e32 v26, 0xbfd9db23, v25
	v_mul_f32_e32 v22, v22, v23
	v_fmamk_f32 v23, v80, 0x3c800000, v16
	v_min_f32_e32 v23, 0x40e00000, v23
	v_mul_f32_e32 v24, 0xbfd9db23, v23
	v_mul_f32_e32 v24, 0x3fb8aa3b, v24
	v_exp_f32_e32 v24, v24
	v_mul_f32_e32 v26, 0x3fb8aa3b, v26
	v_exp_f32_e32 v26, v26
	v_min_f32_e32 v27, 0x40e00000, v27
	v_add_f32_e32 v24, 1.0, v24
	v_rcp_f32_e32 v24, v24
	v_mul_f32_e32 v28, 0xbfd9db23, v27
	v_mul_f32_e32 v28, 0x3fb8aa3b, v28
	v_exp_f32_e32 v28, v28
	v_mul_f32_e32 v23, v23, v24
	v_add_f32_e32 v24, 1.0, v26
	v_rcp_f32_e32 v24, v24
	v_fmamk_f32 v20, v74, 0x3c800000, v10
	v_med3_f32 v20, v20, s57, v196
	v_add_f32_e32 v20, 1.0, v20
	v_mul_f32_e32 v24, v25, v24
	v_fmamk_f32 v25, v70, 0x3c800000, v6
	v_min_f32_e32 v25, 0x40e00000, v25
	v_mul_f32_e32 v26, 0xbfd9db23, v25
	v_mul_f32_e32 v26, 0x3fb8aa3b, v26
	v_exp_f32_e32 v26, v26
	v_mul_f32_e32 v21, v20, v21
	v_fmamk_f32 v20, v75, 0x3c800000, v11
	v_med3_f32 v20, v20, s57, v196
	v_add_f32_e32 v26, 1.0, v26
	v_rcp_f32_e32 v26, v26
	v_add_f32_e32 v20, 1.0, v20
	v_mul_f32_e32 v22, v20, v22
	v_fmamk_f32 v20, v76, 0x3c800000, v12
	v_mul_f32_e32 v25, v25, v26
	v_add_f32_e32 v26, 1.0, v28
	v_rcp_f32_e32 v26, v26
	v_med3_f32 v20, v20, s57, v196
	v_add_f32_e32 v20, 1.0, v20
	v_mul_f32_e32 v23, v20, v23
	v_mul_f32_e32 v26, v27, v26
	v_fmamk_f32 v27, v72, 0x3c800000, v8
	v_min_f32_e32 v27, 0x40e00000, v27
	v_fmamk_f32 v20, v77, 0x3c800000, v13
	v_mul_f32_e32 v28, 0xbfd9db23, v27
	v_med3_f32 v20, v20, s57, v196
	v_mul_f32_e32 v28, 0x3fb8aa3b, v28
	v_add_f32_e32 v20, 1.0, v20
	v_exp_f32_e32 v28, v28
	v_mul_f32_e32 v24, v20, v24
	v_fmamk_f32 v20, v66, 0x3c800000, v2
	v_med3_f32 v20, v20, s57, v196
	v_fmamk_f32 v29, v73, 0x3c800000, v9
	v_add_f32_e32 v20, 1.0, v20
	v_min_f32_e32 v29, 0x40e00000, v29
	v_mul_f32_e32 v25, v20, v25
	v_fmamk_f32 v20, v67, 0x3c800000, v3
	v_add_f32_e32 v28, 1.0, v28
	v_mul_f32_e32 v30, 0xbfd9db23, v29
	v_med3_f32 v20, v20, s57, v196
	v_rcp_f32_e32 v28, v28
	v_mul_f32_e32 v30, 0x3fb8aa3b, v30
	v_add_f32_e32 v20, 1.0, v20
	v_exp_f32_e32 v30, v30
	v_mul_f32_e32 v26, v20, v26
	v_fmamk_f32 v20, v68, 0x3c800000, v4
	v_med3_f32 v20, v20, s57, v196
	v_mul_f32_e32 v27, v27, v28
	v_add_f32_e32 v20, 1.0, v20
	v_add_f32_e32 v28, 1.0, v30
	v_mul_f32_e32 v27, v20, v27
	v_fmamk_f32 v20, v69, 0x3c800000, v5
	v_rcp_f32_e32 v28, v28
	v_med3_f32 v30, v20, s57, v196
	v_mov_b32_e32 v20, v181
	v_cvt_pk_fp8_f32 v20, v21, v22
	v_mov_b32_e32 v21, v181
	v_cvt_pk_fp8_f32 v21, v25, v26
	v_mul_f32_e32 v28, v29, v28
	v_add_f32_e32 v22, 1.0, v30
	v_fmamk_f32 v14, v62, 0x3c800000, v14
	v_mul_f32_e32 v22, v22, v28
	v_min_f32_e32 v14, 0x40e00000, v14
	v_cvt_pk_fp8_f32 v21, v27, v22 op_sel:[0,0,1]
	v_mul_f32_e32 v22, 0xbfd9db23, v14
	v_cvt_pk_fp8_f32 v20, v23, v24 op_sel:[0,0,1]
	v_mul_f32_e32 v22, 0x3fb8aa3b, v22
	v_exp_f32_e32 v24, v22
	v_add_co_u32_e32 v22, vcc, s60, v18
	v_fmamk_f32 v15, v63, 0x3c800000, v15
	s_nop 0
	v_addc_co_u32_e32 v23, vcc, 0, v19, vcc
	v_min_f32_e32 v15, 0x40e00000, v15
	global_store_dwordx2 v[22:23], v[20:21], off
	v_mul_f32_e32 v21, 0xbfd9db23, v15
	v_add_f32_e32 v20, 1.0, v24
	v_mul_f32_e32 v21, 0x3fb8aa3b, v21
	v_rcp_f32_e32 v20, v20
	v_exp_f32_e32 v21, v21
	v_fmamk_f32 v10, v58, 0x3c800000, v10
	v_med3_f32 v10, v10, s57, v196
	v_mul_f32_e32 v14, v14, v20
	v_add_f32_e32 v20, 1.0, v21
	v_rcp_f32_e32 v20, v20
	v_add_f32_e32 v10, 1.0, v10
	v_mul_f32_e32 v10, v10, v14
	v_fmamk_f32 v11, v59, 0x3c800000, v11
	v_mul_f32_e32 v14, v15, v20
	v_fmamk_f32 v15, v64, 0x3c800000, v16
	v_min_f32_e32 v15, 0x40e00000, v15
	v_mul_f32_e32 v16, 0xbfd9db23, v15
	v_mul_f32_e32 v16, 0x3fb8aa3b, v16
	v_exp_f32_e32 v16, v16
	v_med3_f32 v11, v11, s57, v196
	v_add_f32_e32 v11, 1.0, v11
	v_fmac_f32_e32 v17, 0x3c800000, v65
	v_mul_f32_e32 v11, v11, v14
	v_add_f32_e32 v14, 1.0, v16
	v_min_f32_e32 v16, 0x40e00000, v17
	v_mul_f32_e32 v17, 0xbfd9db23, v16
	v_mul_f32_e32 v17, 0x3fb8aa3b, v17
	v_rcp_f32_e32 v14, v14
	v_exp_f32_e32 v17, v17
	v_fmamk_f32 v12, v60, 0x3c800000, v12
	v_med3_f32 v12, v12, s57, v196
	v_mul_f32_e32 v14, v15, v14
	v_add_f32_e32 v15, 1.0, v17
	v_rcp_f32_e32 v15, v15
	v_fmamk_f32 v6, v54, 0x3c800000, v6
	v_add_f32_e32 v12, 1.0, v12
	v_min_f32_e32 v6, 0x40e00000, v6
	v_mul_f32_e32 v12, v12, v14
	v_mul_f32_e32 v14, v16, v15
	v_mul_f32_e32 v15, 0xbfd9db23, v6
	v_mul_f32_e32 v15, 0x3fb8aa3b, v15
	v_exp_f32_e32 v15, v15
	v_fmac_f32_e32 v13, 0x3c800000, v61
	v_med3_f32 v13, v13, s57, v196
	v_fmamk_f32 v7, v55, 0x3c800000, v7
	v_add_f32_e32 v13, 1.0, v13
	v_min_f32_e32 v7, 0x40e00000, v7
	v_mul_f32_e32 v13, v13, v14
	v_add_f32_e32 v14, 1.0, v15
	v_mul_f32_e32 v15, 0xbfd9db23, v7
	v_mul_f32_e32 v15, 0x3fb8aa3b, v15
	v_rcp_f32_e32 v14, v14
	v_exp_f32_e32 v15, v15
	v_fmamk_f32 v2, v50, 0x3c800000, v2
	v_med3_f32 v2, v2, s57, v196
	v_mul_f32_e32 v6, v6, v14
	v_add_f32_e32 v14, 1.0, v15
	v_rcp_f32_e32 v14, v14
	v_add_f32_e32 v2, 1.0, v2
	v_mul_f32_e32 v6, v2, v6
	v_fmamk_f32 v2, v51, 0x3c800000, v3
	v_mul_f32_e32 v3, v7, v14
	v_fmamk_f32 v7, v56, 0x3c800000, v8
	v_min_f32_e32 v7, 0x40e00000, v7
	v_mul_f32_e32 v8, 0xbfd9db23, v7
	v_mul_f32_e32 v8, 0x3fb8aa3b, v8
	v_exp_f32_e32 v8, v8
	v_med3_f32 v2, v2, s57, v196
	v_add_f32_e32 v2, 1.0, v2
	v_fmac_f32_e32 v9, 0x3c800000, v57
	v_mul_f32_e32 v14, v2, v3
	v_fmamk_f32 v2, v52, 0x3c800000, v4
	v_min_f32_e32 v4, 0x40e00000, v9
	v_add_f32_e32 v3, 1.0, v8
	v_mul_f32_e32 v8, 0xbfd9db23, v4
	v_mul_f32_e32 v8, 0x3fb8aa3b, v8
	v_rcp_f32_e32 v3, v3
	v_exp_f32_e32 v8, v8
	v_med3_f32 v2, v2, s57, v196
	v_add_f32_e32 v2, 1.0, v2
	v_mul_f32_e32 v3, v7, v3
	v_add_f32_e32 v7, 1.0, v8
	v_rcp_f32_e32 v7, v7
	v_mul_f32_e32 v8, v2, v3
	v_mov_b32_e32 v2, v181
	v_mov_b32_e32 v3, v181
	v_fmac_f32_e32 v5, 0x3c800000, v53
	v_cvt_pk_fp8_f32 v2, v10, v11
	v_cvt_pk_fp8_f32 v3, v6, v14
	v_med3_f32 v5, v5, s57, v196
	v_mul_f32_e32 v4, v4, v7
	v_add_f32_e32 v5, 1.0, v5
	v_mul_f32_e32 v4, v5, v4
	v_cvt_pk_fp8_f32 v2, v12, v13 op_sel:[0,0,1]
	v_cvt_pk_fp8_f32 v3, v8, v4 op_sel:[0,0,1]
	v_add_co_u32_e32 v4, vcc, 0x58000, v18
	s_nop 1
	v_addc_co_u32_e32 v5, vcc, 0, v19, vcc
	s_and_b64 vcc, exec, s[22:23]
	global_store_dwordx2 v[4:5], v[2:3], off
	s_cbranch_vccnz .LBB0_871

; #define PG8_ROWS(x0, uidx) do { ro[x0] = (unsigned)g.rowtab[(uidx) * 256 + Rl + 64 * (x0)]; ro[(x0) + 1] = (unsigned)g.rowtab[(uidx) * 256 + Rl + 64 * (x0) + 64]; } while (0)
; #define PG8_LDA(dst, b, h) do { _Pragma("unroll") for (int m = 0; m < 4; ++m) { \
;         if constexpr (FP8) dst##8[m] = ld32(lds + PG8_SA(b, h) + aoff0 + m * 2048); \
;         else { dst[m][0] = *(const LAS bf16x8*)(lds + PG8_SA(b, h) + aoff0 + m * 2048); dst[m][1] = *(const LAS bf16x8*)(lds + PG8_SA(b, h) + aoff0 + m * 2048 + 1024); } } } while (0)
; #define PG8_LDB(dst, b, h) do { _Pragma("unroll") for (int n = 0; n < 2; ++n) { \
;         if constexpr (FP8) dst##8[n] = ld32(lds + PG8_SB(b, h) + boff0 + n * 2048); \
;         else { dst[n][0] = *(const LAS bf16x8*)(lds + PG8_SB(b, h) + boff0 + n * 2048); dst[n][1] = *(const LAS bf16x8*)(lds + PG8_SB(b, h) + boff0 + n * 2048 + 1024); } } } while (0)
; #define PG8_SCHED __builtin_amdgcn_sched_barrier(0)
; template <bool FP8, bool GATHER, class Epi, class Sched>
; __device__ __forceinline__ void gemm_phase(LAS unsigned char* lds, const Gemm g, const Sched& S, const Epi& E) {
;     ...
;         for (int t = 0; t < nt; t += 2) {
;             const bool last = (t == nt - 2);
;             const size_t k1 = (size_t)(t + 1) * kstep, k2 = last ? 0 : (size_t)(t + 2) * kstep, k3 = k2 + kstep;
;             const char* b2 = last ? nB : cB + (size_t)(t + 2) * kstep; const char* b3 = b2 + kstep;
;             if constexpr (GATHER) { if (last && has_next) PG8_ROWS(0, ui + 1); }
;             PG8_LDB(B0, 0, 0); PG8_SCHED; PG8_LDA(At, 0, 0); PG8_STAGEA(PG8_SA(1, 1), false, 1, k1);
.LBB0_865:
	s_cmp_eq_u32 s82, 2
	s_cbranch_scc1 .Lcj_865
	s_cmp_lg_u32 s85, 0
	s_cbranch_scc1 .Lsj_865
	s_cmp_eq_u32 s29, 12
	s_cselect_b64 s[42:43], -1, 0
	s_and_b64 s[30:31], s[38:39], s[42:43]
	v_cndmask_b32_e64 v2, 0, 1, s[30:31]
	v_cmp_ne_u32_e64 s[0:1], 1, v2
	s_andn2_b64 vcc, exec, s[30:31]
	s_cbranch_vccnz .LBB0_867
	ds_read2st64_b32 v[182:183], v199 offset1:1

; template <bool FP8, bool GATHER, class Epi, class Sched>
; __device__ __forceinline__ void gemm_phase(LAS unsigned char* lds, const Gemm g, const Sched& S, const Epi& E) {
;     ...
;         for (int t = 0; t < nt; t += 2) {
;             const bool last = (t == nt - 2);
;             const size_t k1 = (size_t)(t + 1) * kstep, k2 = last ? 0 : (size_t)(t + 2) * kstep, k3 = k2 + kstep;
;             const char* b2 = last ? nB : cB + (size_t)(t + 2) * kstep; const char* b3 = b2 + kstep;
;             if constexpr (GATHER) { if (last && has_next) PG8_ROWS(0, ui + 1); }
;             PG8_LDB(B0, 0, 0); PG8_SCHED; PG8_LDA(At, 0, 0); PG8_STAGEA(PG8_SA(1, 1), false, 1, k1);
;             if constexpr (GATHER) { if (last && has_next) PG8_ROWS(2, ui + 1); }
;             PG8_WAIT_V(10); PG8_WAIT_L(8); PG8_BAR; PG8_WAIT_L(0); PG8_MMA(0, 0, At, B0); PG8_BAR; PG8_SCHED;
;             PG8_LDB(B1, 0, 1); PG8_STAGE(PG8_SB(0, 0), b2, voffB);
;             PG8_WAIT_V(10); PG8_BAR; PG8_WAIT_L(0); PG8_MMA(0, 1, At, B1); PG8_BAR;
;             PG8_LDA(At, 0, 1); PG8_STAGEA(PG8_SA(0, 0), last, 0, k2);
;             PG8_BAR; PG8_WAIT_L(0); if (cfull) PG8_MMA(1, 0, At, B0); PG8_BAR; PG8_SCHED;
;             PG8_STAGE(PG8_SB(0, 1), b2 + hstep, voffB);
;             PG8_WAIT_V(10); PG8_BAR; if (cfull) PG8_MMA(1, 1, At, B1); PG8_BAR;
;             PG8_LDB(B0, 1, 0); PG8_SCHED; PG8_LDA(At, 1, 0); PG8_STAGEA(PG8_SA(0, 1), last, 1, k2);
;             PG8_WAIT_V(10); PG8_WAIT_L(8); PG8_BAR; PG8_WAIT_L(0); PG8_MMA(0, 0, At, B0); PG8_BAR; PG8_SCHED;
; __device__ __forceinline__ SJob sjob_addr(const Args& a, int j, int lane) {
;     SJob c; const int kseg = lane & 7, nq = lane >> 3;
;     if (j < SJOBS_GU) { const int e = j >> 12, kb = (j >> 7) & 31, nb = j & 127, s0 = nb * 32, bj = s0 >> 11, rem = s0 & 2047, pn = rem >> 7, c0 = rem & 127, np = pn * 256 + bj * 128 + c0;
;         c.ld = 4096; c.src = a.w_gate_up + ((size_t)e * 2048 + kb * 64 + kseg * 8) * 4096 + s0 + nq * 4; c.dst = (unsigned char*)(a.ws + WS_WGU_T) + ((size_t)e * 4096 + np + nq * 4) * 2048 + kb * 64 + kseg * 8; }
;     else { const int jj = j - SJOBS_GU, e = jj >> 11, kb = (jj >> 6) & 31, nb = jj & 63;
;         c.ld = 2048; c.src = a.w_down + ((size_t)e * 2048 + kb * 64 + kseg * 8) * 2048 + nb * 32 + nq * 4; c.dst = (unsigned char*)(a.ws + WS_WD_T) + ((size_t)e * 2048 + nb * 32 + nq * 4) * 2048 + kb * 64 + kseg * 8; }
.Lsj_869:
	s_lshr_b32 s90, s98, 1
	s_mul_i32 s90, s90, s83
	s_add_i32 s90, s90, s84
	s_lshr_b32 s91, s90, 10
	s_lshl_b32 s91, s91, 11
	s_and_b32 s99, s90, 0x3c0
	s_lshl_b32 s99, s99, 1
	s_or_b32 s91, s91, s99
	s_and_b32 s99, s98, 1
	s_lshl_b32 s99, s99, 6
	s_or_b32 s91, s91, s99
	s_and_b32 s90, s90, 63
	s_or_b32 s90, s90, s91
	s_lshr_b32 s91, s90, 11
	s_and_b32 s99, s90, 0x7c0
	s_and_b32 s82, s90, 63
	s_lshl_b32 s32, s91, 24
	s_lshl_b32 s100, s99, 13
	s_add_i32 s32, s32, s100
	s_lshl_b32 s100, s82, 7
	s_add_i32 s32, s32, s100
	s_add_u32 s100, s86, s32
	s_addc_u32 s101, s87, 0
	s_lshl_b32 s32, s91, 22
	s_lshl_b32 s82, s82, 16
	s_add_i32 s32, s32, s82
	s_add_i32 s32, s32, s99
	s_add_u32 s90, s88, s32
	s_addc_u32 s91, s89, 0
	global_load_dwordx4 v[218:221], v252, s[100:101] nt
	s_add_u32 s100, s100, 0x2000
	s_addc_u32 s101, s101, 0
	global_load_dwordx4 v[222:225], v252, s[100:101] nt
	s_add_u32 s100, s100, 0x2000
	s_addc_u32 s101, s101, 0
	global_load_dwordx4 v[226:229], v252, s[100:101] nt
	s_add_u32 s100, s100, 0x2000
	s_addc_u32 s101, s101, 0
	global_load_dwordx4 v[230:233], v252, s[100:101] nt
	s_add_u32 s100, s100, 0x2000
	s_addc_u32 s101, s101, 0
	global_load_dwordx4 v[234:237], v252, s[100:101] nt
	s_add_u32 s100, s100, 0x2000
	s_addc_u32 s101, s101, 0
	global_load_dwordx4 v[238:241], v252, s[100:101] nt
	s_add_u32 s100, s100, 0x2000
	s_addc_u32 s101, s101, 0
	global_load_dwordx4 v[242:245], v252, s[100:101] nt
	s_add_u32 s100, s100, 0x2000
	s_addc_u32 s101, s101, 0
	global_load_dwordx4 v[246:249], v252, s[100:101] nt
	s_add_u32 s0, s40, 0x100
	s_addc_u32 s1, s41, 0
	s_and_b64 s[30:31], s[42:43], exec
	s_cselect_b32 s2, 0, s0
	s_add_u32 s33, s25, s40
	s_addc_u32 s35, s28, s41
	s_waitcnt vmcnt(22)
	s_and_b64 s[30:31], s[42:43], exec
	s_waitcnt lgkmcnt(8)
	s_barrier
	s_waitcnt lgkmcnt(0)
	s_cselect_b32 s40, s19, s33
	s_cselect_b32 s41, s17, s35
	s_add_u32 s42, s40, 0x80
	v_mov_b32_e32 v187, v181
	s_addc_u32 s43, s41, 0
	s_setprio 1
	s_waitcnt lgkmcnt(0)
	v_mfma_f32_16x16x128_f8f6f4 v[174:177], v[2:9], v[42:49], v[174:177]
	v_mfma_f32_16x16x128_f8f6f4 v[166:169], v[10:17], v[42:49], v[166:169]
	v_mfma_f32_16x16x128_f8f6f4 v[158:161], v[2:9], v[34:41], v[158:161]
	v_mfma_f32_16x16x128_f8f6f4 v[150:153], v[10:17], v[34:41], v[150:153]
	v_mfma_f32_16x16x128_f8f6f4 v[142:145], v[2:9], v[26:33], v[142:145]
	v_mfma_f32_16x16x128_f8f6f4 v[134:137], v[10:17], v[26:33], v[134:137]
	v_mfma_f32_16x16x128_f8f6f4 v[126:129], v[2:9], v[18:25], v[126:129]
	v_mfma_f32_16x16x128_f8f6f4 v[118:121], v[10:17], v[18:25], v[118:121]
	s_setprio 0
	s_barrier
	s_add_i32 s33, 0, 0x14000
	v_add_u32_e32 v212, s33, v197
	s_mov_b64 s[30:31], s[40:41]
	ds_read_b128 v[200:203], v212
	ds_read_b128 v[204:207], v212 offset:1024
	ds_read_b128 v[208:211], v212 offset:2048
	ds_read_b128 v[212:215], v212 offset:3072
	s_mov_b32 m0, s63
	v_lshl_add_u64 v[216:217], s[30:31], 0, v[178:179]
	s_add_u32 s30, s40, 0x20000
	s_addc_u32 s31, s41, 0
	global_load_lds_dwordx4 v[216:217], off
	s_mov_b32 m0, s64
	v_lshl_add_u64 v[216:217], s[30:31], 0, v[178:179]
	global_load_lds_dwordx4 v[216:217], off
	s_waitcnt vmcnt(22)
	s_barrier
	s_waitcnt lgkmcnt(0)
	s_setprio 1
	s_waitcnt lgkmcnt(0)
	v_mfma_f32_16x16x128_f8f6f4 v[170:173], v[200:207], v[42:49], v[170:173]
	v_mfma_f32_16x16x128_f8f6f4 v[162:165], v[208:215], v[42:49], v[162:165]
	v_mfma_f32_16x16x128_f8f6f4 v[154:157], v[200:207], v[34:41], v[154:157]
	v_mfma_f32_16x16x128_f8f6f4 v[146:149], v[208:215], v[34:41], v[146:149]
	v_mfma_f32_16x16x128_f8f6f4 v[138:141], v[200:207], v[26:33], v[138:141]
	v_mfma_f32_16x16x128_f8f6f4 v[130:133], v[208:215], v[26:33], v[130:133]
	v_mfma_f32_16x16x128_f8f6f4 v[122:125], v[200:207], v[18:25], v[122:125]
	v_mfma_f32_16x16x128_f8f6f4 v[114:117], v[208:215], v[18:25], v[114:117]
	s_setprio 0
	s_add_u32 s44, s4, s2
	s_addc_u32 s45, s5, 0
	s_mov_b64 s[30:31], s[44:45]
	s_mov_b32 m0, s37
	s_barrier
	ds_read_b128 v[18:21], v198 offset:16384
	ds_read_b128 v[22:25], v198 offset:17408
	ds_read_b128 v[26:29], v198 offset:18432
	ds_read_b128 v[30:33], v198 offset:19456
	ds_read_b128 v[34:37], v198 offset:20480
	ds_read_b128 v[38:41], v198 offset:21504
	ds_read_b128 v[42:45], v198 offset:22528
	ds_read_b128 v[46:49], v198 offset:23552
	v_add_u32_e32 v216, v182, v191
	global_load_lds_dwordx4 v216, s[30:31]
	s_mov_b64 s[30:31], s[44:45]
	v_add_u32_e32 v217, v183, v191
	s_mov_b32 m0, s65
	s_nop 0
	global_load_lds_dwordx4 v217, s[30:31]
	s_barrier
	s_waitcnt lgkmcnt(0)
	s_setprio 1
	s_waitcnt lgkmcnt(0)
	v_mfma_f32_16x16x128_f8f6f4 v[110:113], v[2:9], v[18:25], v[110:113]
	v_mfma_f32_16x16x128_f8f6f4 v[102:105], v[10:17], v[18:25], v[102:105]
	v_mfma_f32_16x16x128_f8f6f4 v[94:97], v[2:9], v[26:33], v[94:97]
	v_mfma_f32_16x16x128_f8f6f4 v[86:89], v[10:17], v[26:33], v[86:89]
	v_mfma_f32_16x16x128_f8f6f4 v[78:81], v[2:9], v[34:41], v[78:81]
	v_mfma_f32_16x16x128_f8f6f4 v[70:73], v[10:17], v[34:41], v[70:73]
	v_mfma_f32_16x16x128_f8f6f4 v[62:65], v[2:9], v[42:49], v[62:65]
	v_mfma_f32_16x16x128_f8f6f4 v[54:57], v[10:17], v[42:49], v[54:57]
	s_setprio 0
	s_barrier
	s_add_u32 s30, s40, 0x40000
	s_addc_u32 s31, s41, 0
	s_add_i32 s2, s33, s62
	v_lshl_add_u64 v[2:3], s[30:31], 0, v[178:179]
	s_add_u32 s30, s40, 0x60000
	s_mov_b32 m0, s2
	s_addc_u32 s31, s41, 0
	global_load_lds_dwordx4 v[2:3], off
	s_add_i32 m0, s2, 0x2000
	v_lshl_add_u64 v[2:3], s[30:31], 0, v[178:179]
	global_load_lds_dwordx4 v[2:3], off
	s_waitcnt vmcnt(22)
	s_barrier
; #define PG8_STAGE(bufoff, gbase, voff) do { _Pragma("unroll") for (int _i = 0; _i < 2; ++_i) \
;         __builtin_amdgcn_global_load_lds((const unsigned*)(sbase((const char*)(gbase) + _i * pstep) + (voff)), (LAS unsigned*)(lds + (bufoff) + ldsw + _i * 8192), 16, 0, 0); } while (0)
; #define PG8_LDA(dst, b, h) do { _Pragma("unroll") for (int m = 0; m < 4; ++m) { \
;         if constexpr (FP8) dst##8[m] = ld32(lds + PG8_SA(b, h) + aoff0 + m * 2048); \
;         else { dst[m][0] = *(const LAS bf16x8*)(lds + PG8_SA(b, h) + aoff0 + m * 2048); dst[m][1] = *(const LAS bf16x8*)(lds + PG8_SA(b, h) + aoff0 + m * 2048 + 1024); } } } while (0)
; #define PG8_LDB(dst, b, h) do { _Pragma("unroll") for (int n = 0; n < 2; ++n) { \
;         if constexpr (FP8) dst##8[n] = ld32(lds + PG8_SB(b, h) + boff0 + n * 2048); \
;         else { dst[n][0] = *(const LAS bf16x8*)(lds + PG8_SB(b, h) + boff0 + n * 2048); dst[n][1] = *(const LAS bf16x8*)(lds + PG8_SB(b, h) + boff0 + n * 2048 + 1024); } } } while (0)
; #define PG8_WAIT_V(n) asm volatile("s_waitcnt vmcnt(" #n ")" ::: "memory")
; #define PG8_WAIT_L(n) asm volatile("s_waitcnt lgkmcnt(" #n ")" ::: "memory")
; #define PG8_BAR __builtin_amdgcn_s_barrier()
; #define PG8_SCHED __builtin_amdgcn_sched_barrier(0)
; template <bool FP8, bool GATHER, class Epi, class Sched>
; __device__ __forceinline__ void gemm_phase(LAS unsigned char* lds, const Gemm g, const Sched& S, const Epi& E) {
;     ...
;             PG8_WAIT_V(10); PG8_WAIT_L(8); PG8_BAR; PG8_WAIT_L(0); PG8_MMA(0, 0, At, B0); PG8_BAR; PG8_SCHED;
;             PG8_LDB(B1, 1, 1); PG8_STAGE(PG8_SB(1, 0), b3, voffB);
;             PG8_WAIT_V(10); PG8_BAR; PG8_WAIT_L(0); PG8_MMA(0, 1, At, B1); PG8_BAR;
;             PG8_LDA(At, 1, 1); PG8_STAGEA(PG8_SA(1, 0), last, 0, k3);
;             PG8_BAR; PG8_WAIT_L(0); if (cfull) PG8_MMA(1, 0, At, B0); PG8_BAR; PG8_SCHED;
;             PG8_STAGE(PG8_SB(1, 1), b3 + hstep, voffB);
;             PG8_WAIT_V(10); PG8_BAR; if (cfull) PG8_MMA(1, 1, At, B1); PG8_BAR;
; __device__ __forceinline__ void sjob_store(const SJob& c, const f32x4 (&v)[8]) {
; #pragma unroll
;     for (int jn = 0; jn < 4; ++jn) { u32x2 o;
;         o.x = pk4_fp8_scaled(v[0][jn], v[1][jn], v[2][jn], v[3][jn]); o.y = pk4_fp8_scaled(v[4][jn], v[5][jn], v[6][jn], v[7][jn]);
;         __builtin_nontemporal_store(o, (u32x2*)(c.dst + (size_t)jn * 2048)); }
; }
	s_setprio 1
	v_mfma_f32_16x16x128_f8f6f4 v[106:109], v[200:207], v[18:25], v[106:109]
	v_mfma_f32_16x16x128_f8f6f4 v[98:101], v[208:215], v[18:25], v[98:101]
	v_mfma_f32_16x16x128_f8f6f4 v[90:93], v[200:207], v[26:33], v[90:93]
	v_mfma_f32_16x16x128_f8f6f4 v[82:85], v[208:215], v[26:33], v[82:85]
	v_mfma_f32_16x16x128_f8f6f4 v[74:77], v[200:207], v[34:41], v[74:77]
	v_mfma_f32_16x16x128_f8f6f4 v[66:69], v[208:215], v[34:41], v[66:69]
	v_mfma_f32_16x16x128_f8f6f4 v[58:61], v[200:207], v[42:49], v[58:61]
	v_mfma_f32_16x16x128_f8f6f4 v[50:53], v[208:215], v[42:49], v[50:53]
	s_setprio 0
	s_add_i32 s2, 0, 0x18000
	v_add_u32_e32 v14, s2, v197
	s_barrier
	ds_read_b128 v[2:5], v14
	ds_read_b128 v[6:9], v14 offset:1024
	ds_read_b128 v[10:13], v14 offset:2048
	ds_read_b128 v[14:17], v14 offset:3072
	s_mov_b64 s[30:31], s[44:45]
	ds_read_b128 v[18:21], v198 offset:32768
	ds_read_b128 v[22:25], v198 offset:33792
	ds_read_b128 v[26:29], v198 offset:34816
	ds_read_b128 v[30:33], v198 offset:35840
	ds_read_b128 v[34:37], v198 offset:36864
	ds_read_b128 v[38:41], v198 offset:37888
	ds_read_b128 v[42:45], v198 offset:38912
	ds_read_b128 v[46:49], v198 offset:39936
	s_mov_b32 m0, s66
	v_lshl_add_u64 v[200:201], s[30:31], 0, v[180:181]
	s_mov_b64 s[30:31], s[44:45]
	global_load_lds_dwordx4 v[200:201], off
	s_mov_b32 m0, s67
	v_lshl_add_u64 v[186:187], s[30:31], 0, v[186:187]
	global_load_lds_dwordx4 v[186:187], off
	s_waitcnt vmcnt(22)
	s_waitcnt lgkmcnt(8)
	s_barrier
	s_waitcnt lgkmcnt(0)
	s_setprio 1
	s_waitcnt lgkmcnt(0)
	v_mfma_f32_16x16x128_f8f6f4 v[174:177], v[2:9], v[18:25], v[174:177]
	v_mfma_f32_16x16x128_f8f6f4 v[166:169], v[10:17], v[18:25], v[166:169]
	v_mfma_f32_16x16x128_f8f6f4 v[158:161], v[2:9], v[26:33], v[158:161]
	v_mfma_f32_16x16x128_f8f6f4 v[150:153], v[10:17], v[26:33], v[150:153]
	v_mfma_f32_16x16x128_f8f6f4 v[142:145], v[2:9], v[34:41], v[142:145]
	v_mfma_f32_16x16x128_f8f6f4 v[134:137], v[10:17], v[34:41], v[134:137]
	v_mfma_f32_16x16x128_f8f6f4 v[126:129], v[2:9], v[42:49], v[126:129]
	v_mfma_f32_16x16x128_f8f6f4 v[118:121], v[10:17], v[42:49], v[118:121]
	s_setprio 0
	s_barrier
	s_add_i32 s33, 0, 0x1c000
	s_add_i32 s2, s2, s62
	v_add_u32_e32 v180, s33, v197
	s_add_u32 s30, s40, 0x20080
	ds_read_b128 v[200:203], v180
	ds_read_b128 v[204:207], v180 offset:1024
	ds_read_b128 v[208:211], v180 offset:2048
	ds_read_b128 v[212:215], v180 offset:3072
	s_mov_b32 m0, s2
	v_lshl_add_u64 v[186:187], s[42:43], 0, v[178:179]
	s_addc_u32 s31, s41, 0
	global_load_lds_dwordx4 v[186:187], off
	s_add_i32 m0, s2, 0x2000
	v_lshl_add_u64 v[186:187], s[30:31], 0, v[178:179]
	global_load_lds_dwordx4 v[186:187], off
	s_waitcnt vmcnt(18)
	s_barrier
	s_waitcnt lgkmcnt(0)
	s_setprio 1
	s_waitcnt lgkmcnt(0)
	v_mfma_f32_16x16x128_f8f6f4 v[170:173], v[200:207], v[18:25], v[170:173]
	v_mfma_f32_16x16x128_f8f6f4 v[162:165], v[208:215], v[18:25], v[162:165]
	v_mfma_f32_16x16x128_f8f6f4 v[154:157], v[200:207], v[26:33], v[154:157]
	v_mfma_f32_16x16x128_f8f6f4 v[146:149], v[208:215], v[26:33], v[146:149]
	v_mfma_f32_16x16x128_f8f6f4 v[138:141], v[200:207], v[34:41], v[138:141]
	v_mfma_f32_16x16x128_f8f6f4 v[130:133], v[208:215], v[34:41], v[130:133]
	v_mfma_f32_16x16x128_f8f6f4 v[122:125], v[200:207], v[42:49], v[122:125]
	v_mfma_f32_16x16x128_f8f6f4 v[114:117], v[208:215], v[42:49], v[114:117]
	s_setprio 0
	s_add_u32 s30, s44, 0x80
	s_addc_u32 s31, s45, 0
	s_mov_b64 s[42:43], s[30:31]
	s_mov_b32 m0, s78
	s_barrier
	ds_read_b128 v[18:21], v198 offset:49152
	ds_read_b128 v[22:25], v198 offset:50176
	ds_read_b128 v[26:29], v198 offset:51200
	ds_read_b128 v[30:33], v198 offset:52224
	ds_read_b128 v[34:37], v198 offset:53248
	ds_read_b128 v[38:41], v198 offset:54272
	ds_read_b128 v[42:45], v198 offset:55296
	ds_read_b128 v[46:49], v198 offset:56320
	s_nop 0
	global_load_lds_dwordx4 v216, s[42:43]
	s_mov_b32 m0, s79
	s_nop 0
	global_load_lds_dwordx4 v217, s[30:31]
	s_barrier
	s_waitcnt lgkmcnt(0)
	s_setprio 1
	s_waitcnt lgkmcnt(0)
	v_mfma_f32_16x16x128_f8f6f4 v[110:113], v[2:9], v[18:25], v[110:113]
	v_mfma_f32_16x16x128_f8f6f4 v[102:105], v[10:17], v[18:25], v[102:105]
	v_mfma_f32_16x16x128_f8f6f4 v[94:97], v[2:9], v[26:33], v[94:97]
	v_mfma_f32_16x16x128_f8f6f4 v[86:89], v[10:17], v[26:33], v[86:89]
	v_mfma_f32_16x16x128_f8f6f4 v[78:81], v[2:9], v[34:41], v[78:81]
	v_mfma_f32_16x16x128_f8f6f4 v[70:73], v[10:17], v[34:41], v[70:73]
	v_mfma_f32_16x16x128_f8f6f4 v[62:65], v[2:9], v[42:49], v[62:65]
	v_mfma_f32_16x16x128_f8f6f4 v[54:57], v[10:17], v[42:49], v[54:57]
	s_setprio 0
	s_barrier
	s_add_u32 s30, s40, 0x40080
	s_addc_u32 s31, s41, 0
	s_add_i32 s2, s33, s62
	v_lshl_add_u64 v[2:3], s[30:31], 0, v[178:179]
	s_add_u32 s30, s40, 0x60080
	s_mov_b32 m0, s2
	s_addc_u32 s31, s41, 0
	global_load_lds_dwordx4 v[2:3], off
	s_add_i32 m0, s2, 0x2000
	v_lshl_add_u64 v[2:3], s[30:31], 0, v[178:179]
	global_load_lds_dwordx4 v[2:3], off
	s_waitcnt vmcnt(10)
	v_cvt_scalef32_pk_fp8_f32 v250, v218, v222, v254
	v_cvt_scalef32_pk_fp8_f32 v251, v234, v238, v254
	v_cvt_scalef32_pk_fp8_f32 v250, v226, v230, v254 op_sel:[0,0,0,1]
	v_cvt_scalef32_pk_fp8_f32 v251, v242, v246, v254 op_sel:[0,0,0,1]
	global_store_dwordx2 v253, v[250:251], s[90:91] nt
	v_cvt_scalef32_pk_fp8_f32 v250, v219, v223, v254
	v_cvt_scalef32_pk_fp8_f32 v251, v235, v239, v254
	v_cvt_scalef32_pk_fp8_f32 v250, v227, v231, v254 op_sel:[0,0,0,1]
	v_cvt_scalef32_pk_fp8_f32 v251, v243, v247, v254 op_sel:[0,0,0,1]
	global_store_dwordx2 v253, v[250:251], s[90:91] offset:2048 nt
	v_cvt_scalef32_pk_fp8_f32 v250, v220, v224, v254
	v_cvt_scalef32_pk_fp8_f32 v251, v236, v240, v254
	v_cvt_scalef32_pk_fp8_f32 v250, v228, v232, v254 op_sel:[0,0,0,1]
	v_cvt_scalef32_pk_fp8_f32 v251, v244, v248, v254 op_sel:[0,0,0,1]
	s_add_u32 s90, s90, 0x1000
	s_addc_u32 s91, s91, 0
	global_store_dwordx2 v253, v[250:251], s[90:91] nt
	v_cvt_scalef32_pk_fp8_f32 v250, v221, v225, v254
	v_cvt_scalef32_pk_fp8_f32 v251, v237, v241, v254
	v_cvt_scalef32_pk_fp8_f32 v250, v229, v233, v254 op_sel:[0,0,0,1]
	v_cvt_scalef32_pk_fp8_f32 v251, v245, v249, v254 op_sel:[0,0,0,1]
	global_store_dwordx2 v253, v[250:251], s[90:91] offset:2048 nt
	s_add_i32 s98, s98, 1
	s_barrier
	s_setprio 1
	v_mfma_f32_16x16x128_f8f6f4 v[106:109], v[200:207], v[18:25], v[106:109]
	v_mfma_f32_16x16x128_f8f6f4 v[98:101], v[208:215], v[18:25], v[98:101]
	v_mfma_f32_16x16x128_f8f6f4 v[90:93], v[200:207], v[26:33], v[90:93]
	v_mfma_f32_16x16x128_f8f6f4 v[82:85], v[208:215], v[26:33], v[82:85]
	v_mfma_f32_16x16x128_f8f6f4 v[74:77], v[200:207], v[34:41], v[74:77]
	v_mfma_f32_16x16x128_f8f6f4 v[66:69], v[208:215], v[34:41], v[66:69]
	v_mfma_f32_16x16x128_f8f6f4 v[58:61], v[200:207], v[42:49], v[58:61]
	v_mfma_f32_16x16x128_f8f6f4 v[50:53], v[208:215], v[42:49], v[50:53]
	s_setprio 0
	s_add_i32 s29, s29, 2
	s_cmp_gt_u32 s29, 13
	s_barrier
	s_cbranch_scc1 .LBB0_853
	s_mov_b64 s[40:41], s[0:1]
	s_branch .Lsj_865
; #define PG8_ROWS(x0, uidx) do { ro[x0] = (unsigned)g.rowtab[(uidx) * 256 + Rl + 64 * (x0)]; ro[(x0) + 1] = (unsigned)g.rowtab[(uidx) * 256 + Rl + 64 * (x0) + 64]; } while (0)
; #define PG8_LDA(dst, b, h) do { _Pragma("unroll") for (int m = 0; m < 4; ++m) { \
;         if constexpr (FP8) dst##8[m] = ld32(lds + PG8_SA(b, h) + aoff0 + m * 2048); \
;         else { dst[m][0] = *(const LAS bf16x8*)(lds + PG8_SA(b, h) + aoff0 + m * 2048); dst[m][1] = *(const LAS bf16x8*)(lds + PG8_SA(b, h) + aoff0 + m * 2048 + 1024); } } } while (0)
; #define PG8_LDB(dst, b, h) do { _Pragma("unroll") for (int n = 0; n < 2; ++n) { \
;         if constexpr (FP8) dst##8[n] = ld32(lds + PG8_SB(b, h) + boff0 + n * 2048); \
;         else { dst[n][0] = *(const LAS bf16x8*)(lds + PG8_SB(b, h) + boff0 + n * 2048); dst[n][1] = *(const LAS bf16x8*)(lds + PG8_SB(b, h) + boff0 + n * 2048 + 1024); } } } while (0)
; #define PG8_SCHED __builtin_amdgcn_sched_barrier(0)
; template <bool FP8, bool GATHER, class Epi, class Sched>
; __device__ __forceinline__ void gemm_phase(LAS unsigned char* lds, const Gemm g, const Sched& S, const Epi& E) {
;     ...
;             if constexpr (GATHER) { if (last && has_next) PG8_ROWS(0, ui + 1); }
;             PG8_LDB(B0, 0, 0); PG8_SCHED; PG8_LDA(At, 0, 0); PG8_STAGEA(PG8_SA(1, 1), false, 1, k1);
.Lcj_865:
	s_cmp_eq_u32 s29, 12
	s_cselect_b64 s[42:43], -1, 0
	s_and_b64 s[30:31], s[38:39], s[42:43]
	v_cndmask_b32_e64 v2, 0, 1, s[30:31]
	v_cmp_ne_u32_e64 s[0:1], 1, v2
	s_andn2_b64 vcc, exec, s[30:31]
	s_cbranch_vccnz .Lcj_867
	ds_read2st64_b32 v[182:183], v199 offset1:1

; #define PG8_ROWS(x0, uidx) do { ro[x0] = (unsigned)g.rowtab[(uidx) * 256 + Rl + 64 * (x0)]; ro[(x0) + 1] = (unsigned)g.rowtab[(uidx) * 256 + Rl + 64 * (x0) + 64]; } while (0)
; #define PG8_STAGE(bufoff, gbase, voff) do { _Pragma("unroll") for (int _i = 0; _i < 2; ++_i) \
;         __builtin_amdgcn_global_load_lds((const unsigned*)(sbase((const char*)(gbase) + _i * pstep) + (voff)), (LAS unsigned*)(lds + (bufoff) + ldsw + _i * 8192), 16, 0, 0); } while (0)
; #define PG8_LDA(dst, b, h) do { _Pragma("unroll") for (int m = 0; m < 4; ++m) { \
;         if constexpr (FP8) dst##8[m] = ld32(lds + PG8_SA(b, h) + aoff0 + m * 2048); \
;         else { dst[m][0] = *(const LAS bf16x8*)(lds + PG8_SA(b, h) + aoff0 + m * 2048); dst[m][1] = *(const LAS bf16x8*)(lds + PG8_SA(b, h) + aoff0 + m * 2048 + 1024); } } } while (0)
; #define PG8_LDB(dst, b, h) do { _Pragma("unroll") for (int n = 0; n < 2; ++n) { \
;         if constexpr (FP8) dst##8[n] = ld32(lds + PG8_SB(b, h) + boff0 + n * 2048); \
;         else { dst[n][0] = *(const LAS bf16x8*)(lds + PG8_SB(b, h) + boff0 + n * 2048); dst[n][1] = *(const LAS bf16x8*)(lds + PG8_SB(b, h) + boff0 + n * 2048 + 1024); } } } while (0)
; #define PG8_WAIT_V(n) asm volatile("s_waitcnt vmcnt(" #n ")" ::: "memory")
; template <bool FP8, bool GATHER, class Epi, class Sched>
; __device__ __forceinline__ void gemm_phase(LAS unsigned char* lds, const Gemm g, const Sched& S, const Epi& E) {
;     ...
;             PG8_LDB(B0, 0, 0); PG8_SCHED; PG8_LDA(At, 0, 0); PG8_STAGEA(PG8_SA(1, 1), false, 1, k1);
;             if constexpr (GATHER) { if (last && has_next) PG8_ROWS(2, ui + 1); }
;             PG8_WAIT_V(10); PG8_WAIT_L(8); PG8_BAR; PG8_WAIT_L(0); PG8_MMA(0, 0, At, B0); PG8_BAR; PG8_SCHED;
;             PG8_LDB(B1, 0, 1); PG8_STAGE(PG8_SB(0, 0), b2, voffB);
;             PG8_WAIT_V(10); PG8_BAR; PG8_WAIT_L(0); PG8_MMA(0, 1, At, B1); PG8_BAR;
;             PG8_LDA(At, 0, 1); PG8_STAGEA(PG8_SA(0, 0), last, 0, k2);
;             PG8_BAR; PG8_WAIT_L(0); if (cfull) PG8_MMA(1, 0, At, B0); PG8_BAR; PG8_SCHED;
;             PG8_STAGE(PG8_SB(0, 1), b2 + hstep, voffB);
;             PG8_WAIT_V(10); PG8_BAR; if (cfull) PG8_MMA(1, 1, At, B1); PG8_BAR;
;             PG8_LDB(B0, 1, 0); PG8_SCHED; PG8_LDA(At, 1, 0); PG8_STAGEA(PG8_SA(0, 1), last, 1, k2);
;             PG8_WAIT_V(10); PG8_WAIT_L(8); PG8_BAR; PG8_WAIT_L(0); PG8_MMA(0, 0, At, B0); PG8_BAR; PG8_SCHED;
.Lcj_869:
	s_add_u32 s0, s40, 0x100
	s_addc_u32 s1, s41, 0
	s_and_b64 s[30:31], s[42:43], exec
	s_cselect_b32 s2, 0, s0
	s_add_u32 s33, s25, s40
	s_addc_u32 s35, s28, s41
	s_waitcnt vmcnt(63)
	s_and_b64 s[30:31], s[42:43], exec
	s_waitcnt lgkmcnt(8)
	s_barrier
	s_waitcnt lgkmcnt(0)
	s_cselect_b32 s40, s19, s33
	s_cselect_b32 s41, s17, s35
	s_add_u32 s42, s40, 0x80
	v_mov_b32_e32 v187, v181
	s_addc_u32 s43, s41, 0
	s_setprio 1
	s_waitcnt lgkmcnt(0)
	v_mfma_f32_16x16x128_f8f6f4 v[174:177], v[2:9], v[42:49], v[174:177]
	v_mfma_f32_16x16x128_f8f6f4 v[166:169], v[10:17], v[42:49], v[166:169]
	v_mfma_f32_16x16x128_f8f6f4 v[158:161], v[2:9], v[34:41], v[158:161]
	v_mfma_f32_16x16x128_f8f6f4 v[150:153], v[10:17], v[34:41], v[150:153]
	v_mfma_f32_16x16x128_f8f6f4 v[142:145], v[2:9], v[26:33], v[142:145]
	v_mfma_f32_16x16x128_f8f6f4 v[134:137], v[10:17], v[26:33], v[134:137]
	v_mfma_f32_16x16x128_f8f6f4 v[126:129], v[2:9], v[18:25], v[126:129]
	v_mfma_f32_16x16x128_f8f6f4 v[118:121], v[10:17], v[18:25], v[118:121]
	s_setprio 0
	s_barrier
	s_add_i32 s33, 0, 0x14000
	v_add_u32_e32 v212, s33, v197
	s_mov_b64 s[30:31], s[40:41]
	ds_read_b128 v[200:203], v212
	ds_read_b128 v[204:207], v212 offset:1024
	ds_read_b128 v[208:211], v212 offset:2048
	ds_read_b128 v[212:215], v212 offset:3072
	s_mov_b32 m0, s63
	v_lshl_add_u64 v[216:217], s[30:31], 0, v[178:179]
	s_add_u32 s30, s40, 0x20000
	s_addc_u32 s31, s41, 0
	global_load_lds_dwordx4 v[216:217], off
	s_mov_b32 m0, s64
	v_lshl_add_u64 v[216:217], s[30:31], 0, v[178:179]
	global_load_lds_dwordx4 v[216:217], off
	s_waitcnt vmcnt(63)
	s_barrier
	s_waitcnt lgkmcnt(0)
	s_setprio 1
	s_waitcnt lgkmcnt(0)
	v_mfma_f32_16x16x128_f8f6f4 v[170:173], v[200:207], v[42:49], v[170:173]
	v_mfma_f32_16x16x128_f8f6f4 v[162:165], v[208:215], v[42:49], v[162:165]
	v_mfma_f32_16x16x128_f8f6f4 v[154:157], v[200:207], v[34:41], v[154:157]
	v_mfma_f32_16x16x128_f8f6f4 v[146:149], v[208:215], v[34:41], v[146:149]
	v_mfma_f32_16x16x128_f8f6f4 v[138:141], v[200:207], v[26:33], v[138:141]
	v_mfma_f32_16x16x128_f8f6f4 v[130:133], v[208:215], v[26:33], v[130:133]
	v_mfma_f32_16x16x128_f8f6f4 v[122:125], v[200:207], v[18:25], v[122:125]
	v_mfma_f32_16x16x128_f8f6f4 v[114:117], v[208:215], v[18:25], v[114:117]
	s_setprio 0
	s_add_u32 s44, s4, s2
	s_addc_u32 s45, s5, 0
	s_mov_b64 s[30:31], s[44:45]
	s_mov_b32 m0, s37
	s_barrier
	ds_read_b128 v[18:21], v198 offset:16384
	ds_read_b128 v[22:25], v198 offset:17408
	ds_read_b128 v[26:29], v198 offset:18432
	ds_read_b128 v[30:33], v198 offset:19456
	ds_read_b128 v[34:37], v198 offset:20480
	ds_read_b128 v[38:41], v198 offset:21504
	ds_read_b128 v[42:45], v198 offset:22528
	ds_read_b128 v[46:49], v198 offset:23552
	v_add_u32_e32 v216, v182, v191
	global_load_lds_dwordx4 v216, s[30:31]
	s_mov_b64 s[30:31], s[44:45]
	v_add_u32_e32 v217, v183, v191
	s_mov_b32 m0, s65
	s_nop 0
	global_load_lds_dwordx4 v217, s[30:31]
	s_barrier
	s_waitcnt lgkmcnt(0)
	s_setprio 1
	s_waitcnt lgkmcnt(0)
	v_mfma_f32_16x16x128_f8f6f4 v[110:113], v[2:9], v[18:25], v[110:113]
	v_mfma_f32_16x16x128_f8f6f4 v[102:105], v[10:17], v[18:25], v[102:105]
	v_mfma_f32_16x16x128_f8f6f4 v[94:97], v[2:9], v[26:33], v[94:97]
	v_mfma_f32_16x16x128_f8f6f4 v[86:89], v[10:17], v[26:33], v[86:89]
	v_mfma_f32_16x16x128_f8f6f4 v[78:81], v[2:9], v[34:41], v[78:81]
	v_mfma_f32_16x16x128_f8f6f4 v[70:73], v[10:17], v[34:41], v[70:73]
	v_mfma_f32_16x16x128_f8f6f4 v[62:65], v[2:9], v[42:49], v[62:65]
	v_mfma_f32_16x16x128_f8f6f4 v[54:57], v[10:17], v[42:49], v[54:57]
	s_setprio 0
	s_barrier
	s_add_u32 s30, s40, 0x40000
	s_addc_u32 s31, s41, 0
	s_add_i32 s2, s33, s62
	v_lshl_add_u64 v[2:3], s[30:31], 0, v[178:179]
	s_add_u32 s30, s40, 0x60000
	s_mov_b32 m0, s2
	s_addc_u32 s31, s41, 0
	global_load_lds_dwordx4 v[2:3], off
	s_add_i32 m0, s2, 0x2000
	v_lshl_add_u64 v[2:3], s[30:31], 0, v[178:179]
	global_load_lds_dwordx4 v[2:3], off
	s_waitcnt vmcnt(63)
	s_barrier
	s_setprio 1
	v_mfma_f32_16x16x128_f8f6f4 v[106:109], v[200:207], v[18:25], v[106:109]
	v_mfma_f32_16x16x128_f8f6f4 v[98:101], v[208:215], v[18:25], v[98:101]
	v_mfma_f32_16x16x128_f8f6f4 v[90:93], v[200:207], v[26:33], v[90:93]
	v_mfma_f32_16x16x128_f8f6f4 v[82:85], v[208:215], v[26:33], v[82:85]
	v_mfma_f32_16x16x128_f8f6f4 v[74:77], v[200:207], v[34:41], v[74:77]
	v_mfma_f32_16x16x128_f8f6f4 v[66:69], v[208:215], v[34:41], v[66:69]
	v_mfma_f32_16x16x128_f8f6f4 v[58:61], v[200:207], v[42:49], v[58:61]
	v_mfma_f32_16x16x128_f8f6f4 v[50:53], v[208:215], v[42:49], v[50:53]
	s_setprio 0
	s_add_i32 s2, 0, 0x18000
	v_add_u32_e32 v14, s2, v197
	s_barrier
	ds_read_b128 v[2:5], v14
	ds_read_b128 v[6:9], v14 offset:1024
	ds_read_b128 v[10:13], v14 offset:2048
	ds_read_b128 v[14:17], v14 offset:3072
	s_mov_b64 s[30:31], s[44:45]
	ds_read_b128 v[18:21], v198 offset:32768
	ds_read_b128 v[22:25], v198 offset:33792
	ds_read_b128 v[26:29], v198 offset:34816
	ds_read_b128 v[30:33], v198 offset:35840
	ds_read_b128 v[34:37], v198 offset:36864
	ds_read_b128 v[38:41], v198 offset:37888
	ds_read_b128 v[42:45], v198 offset:38912
	ds_read_b128 v[46:49], v198 offset:39936
	s_mov_b32 m0, s66
	v_lshl_add_u64 v[200:201], s[30:31], 0, v[180:181]
	s_mov_b64 s[30:31], s[44:45]
	global_load_lds_dwordx4 v[200:201], off
	s_mov_b32 m0, s67
	v_lshl_add_u64 v[186:187], s[30:31], 0, v[186:187]
	global_load_lds_dwordx4 v[186:187], off
	s_waitcnt vmcnt(63)
	s_waitcnt lgkmcnt(8)
	s_barrier
; #define PG8_STAGE(bufoff, gbase, voff) do { _Pragma("unroll") for (int _i = 0; _i < 2; ++_i) \
;         __builtin_amdgcn_global_load_lds((const unsigned*)(sbase((const char*)(gbase) + _i * pstep) + (voff)), (LAS unsigned*)(lds + (bufoff) + ldsw + _i * 8192), 16, 0, 0); } while (0)
; #define PG8_LDA(dst, b, h) do { _Pragma("unroll") for (int m = 0; m < 4; ++m) { \
;         if constexpr (FP8) dst##8[m] = ld32(lds + PG8_SA(b, h) + aoff0 + m * 2048); \
;         else { dst[m][0] = *(const LAS bf16x8*)(lds + PG8_SA(b, h) + aoff0 + m * 2048); dst[m][1] = *(const LAS bf16x8*)(lds + PG8_SA(b, h) + aoff0 + m * 2048 + 1024); } } } while (0)
; #define PG8_LDB(dst, b, h) do { _Pragma("unroll") for (int n = 0; n < 2; ++n) { \
;         if constexpr (FP8) dst##8[n] = ld32(lds + PG8_SB(b, h) + boff0 + n * 2048); \
;         else { dst[n][0] = *(const LAS bf16x8*)(lds + PG8_SB(b, h) + boff0 + n * 2048); dst[n][1] = *(const LAS bf16x8*)(lds + PG8_SB(b, h) + boff0 + n * 2048 + 1024); } } } while (0)
; #define PG8_WAIT_V(n) asm volatile("s_waitcnt vmcnt(" #n ")" ::: "memory")
; #define PG8_WAIT_L(n) asm volatile("s_waitcnt lgkmcnt(" #n ")" ::: "memory")
; #define PG8_BAR __builtin_amdgcn_s_barrier()
; #define PG8_SCHED __builtin_amdgcn_sched_barrier(0)
; template <bool FP8, bool GATHER, class Epi, class Sched>
; __device__ __forceinline__ void gemm_phase(LAS unsigned char* lds, const Gemm g, const Sched& S, const Epi& E) {
;     ...
;             PG8_WAIT_V(10); PG8_WAIT_L(8); PG8_BAR; PG8_WAIT_L(0); PG8_MMA(0, 0, At, B0); PG8_BAR; PG8_SCHED;
;             PG8_LDB(B1, 1, 1); PG8_STAGE(PG8_SB(1, 0), b3, voffB);
;             PG8_WAIT_V(10); PG8_BAR; PG8_WAIT_L(0); PG8_MMA(0, 1, At, B1); PG8_BAR;
;             PG8_LDA(At, 1, 1); PG8_STAGEA(PG8_SA(1, 0), last, 0, k3);
;             PG8_BAR; PG8_WAIT_L(0); if (cfull) PG8_MMA(1, 0, At, B0); PG8_BAR; PG8_SCHED;
;             PG8_STAGE(PG8_SB(1, 1), b3 + hstep, voffB);
;             PG8_WAIT_V(10); PG8_BAR; if (cfull) PG8_MMA(1, 1, At, B1); PG8_BAR;
; __device__ __forceinline__ void sjob_store(const SJob& c, const f32x4 (&v)[8]) {
; #pragma unroll
;     for (int jn = 0; jn < 4; ++jn) { u32x2 o;
;         o.x = pk4_fp8_scaled(v[0][jn], v[1][jn], v[2][jn], v[3][jn]); o.y = pk4_fp8_scaled(v[4][jn], v[5][jn], v[6][jn], v[7][jn]);
;         __builtin_nontemporal_store(o, (u32x2*)(c.dst + (size_t)jn * 2048)); }
; }
	s_waitcnt lgkmcnt(0)
	s_setprio 1
	s_waitcnt lgkmcnt(0)
	v_mfma_f32_16x16x128_f8f6f4 v[174:177], v[2:9], v[18:25], v[174:177]
	v_mfma_f32_16x16x128_f8f6f4 v[166:169], v[10:17], v[18:25], v[166:169]
	v_mfma_f32_16x16x128_f8f6f4 v[158:161], v[2:9], v[26:33], v[158:161]
	v_mfma_f32_16x16x128_f8f6f4 v[150:153], v[10:17], v[26:33], v[150:153]
	v_mfma_f32_16x16x128_f8f6f4 v[142:145], v[2:9], v[34:41], v[142:145]
	v_mfma_f32_16x16x128_f8f6f4 v[134:137], v[10:17], v[34:41], v[134:137]
	v_mfma_f32_16x16x128_f8f6f4 v[126:129], v[2:9], v[42:49], v[126:129]
	v_mfma_f32_16x16x128_f8f6f4 v[118:121], v[10:17], v[42:49], v[118:121]
	s_setprio 0
	s_barrier
	s_add_i32 s33, 0, 0x1c000
	s_add_i32 s2, s2, s62
	v_add_u32_e32 v180, s33, v197
	s_add_u32 s30, s40, 0x20080
	ds_read_b128 v[200:203], v180
	ds_read_b128 v[204:207], v180 offset:1024
	ds_read_b128 v[208:211], v180 offset:2048
	ds_read_b128 v[212:215], v180 offset:3072
	s_mov_b32 m0, s2
	v_lshl_add_u64 v[186:187], s[42:43], 0, v[178:179]
	s_addc_u32 s31, s41, 0
	global_load_lds_dwordx4 v[186:187], off
	s_add_i32 m0, s2, 0x2000
	v_lshl_add_u64 v[186:187], s[30:31], 0, v[178:179]
	global_load_lds_dwordx4 v[186:187], off
	s_waitcnt vmcnt(10)
	s_barrier
	s_waitcnt lgkmcnt(0)
	s_setprio 1
	s_waitcnt lgkmcnt(0)
	v_mfma_f32_16x16x128_f8f6f4 v[170:173], v[200:207], v[18:25], v[170:173]
	v_mfma_f32_16x16x128_f8f6f4 v[162:165], v[208:215], v[18:25], v[162:165]
	v_mfma_f32_16x16x128_f8f6f4 v[154:157], v[200:207], v[26:33], v[154:157]
	v_mfma_f32_16x16x128_f8f6f4 v[146:149], v[208:215], v[26:33], v[146:149]
	v_mfma_f32_16x16x128_f8f6f4 v[138:141], v[200:207], v[34:41], v[138:141]
	v_mfma_f32_16x16x128_f8f6f4 v[130:133], v[208:215], v[34:41], v[130:133]
	v_mfma_f32_16x16x128_f8f6f4 v[122:125], v[200:207], v[42:49], v[122:125]
	v_mfma_f32_16x16x128_f8f6f4 v[114:117], v[208:215], v[42:49], v[114:117]
	s_setprio 0
	s_add_u32 s30, s44, 0x80
	s_addc_u32 s31, s45, 0
	s_mov_b64 s[42:43], s[30:31]
	s_mov_b32 m0, s78
	s_barrier
	ds_read_b128 v[18:21], v198 offset:49152
	ds_read_b128 v[22:25], v198 offset:50176
	ds_read_b128 v[26:29], v198 offset:51200
	ds_read_b128 v[30:33], v198 offset:52224
	ds_read_b128 v[34:37], v198 offset:53248
	ds_read_b128 v[38:41], v198 offset:54272
	ds_read_b128 v[42:45], v198 offset:55296
	ds_read_b128 v[46:49], v198 offset:56320
	s_nop 0
	global_load_lds_dwordx4 v216, s[42:43]
	s_mov_b32 m0, s79
	s_nop 0
	global_load_lds_dwordx4 v217, s[30:31]
	s_barrier
	s_waitcnt lgkmcnt(0)
	s_setprio 1
	s_waitcnt lgkmcnt(0)
	v_mfma_f32_16x16x128_f8f6f4 v[110:113], v[2:9], v[18:25], v[110:113]
	v_mfma_f32_16x16x128_f8f6f4 v[102:105], v[10:17], v[18:25], v[102:105]
	v_mfma_f32_16x16x128_f8f6f4 v[94:97], v[2:9], v[26:33], v[94:97]
	v_mfma_f32_16x16x128_f8f6f4 v[86:89], v[10:17], v[26:33], v[86:89]
	v_mfma_f32_16x16x128_f8f6f4 v[78:81], v[2:9], v[34:41], v[78:81]
	v_mfma_f32_16x16x128_f8f6f4 v[70:73], v[10:17], v[34:41], v[70:73]
	v_mfma_f32_16x16x128_f8f6f4 v[62:65], v[2:9], v[42:49], v[62:65]
	v_mfma_f32_16x16x128_f8f6f4 v[54:57], v[10:17], v[42:49], v[54:57]
	s_setprio 0
	s_barrier
	s_add_u32 s30, s40, 0x40080
	s_addc_u32 s31, s41, 0
	s_add_i32 s2, s33, s62
	v_lshl_add_u64 v[2:3], s[30:31], 0, v[178:179]
	s_add_u32 s30, s40, 0x60080
	s_mov_b32 m0, s2
	s_addc_u32 s31, s41, 0
	global_load_lds_dwordx4 v[2:3], off
	s_add_i32 m0, s2, 0x2000
	v_lshl_add_u64 v[2:3], s[30:31], 0, v[178:179]
	global_load_lds_dwordx4 v[2:3], off
	s_waitcnt vmcnt(10)
	v_cvt_scalef32_pk_fp8_f32 v250, v218, v222, v254
	v_cvt_scalef32_pk_fp8_f32 v251, v234, v238, v254
	v_cvt_scalef32_pk_fp8_f32 v250, v226, v230, v254 op_sel:[0,0,0,1]
	v_cvt_scalef32_pk_fp8_f32 v251, v242, v246, v254 op_sel:[0,0,0,1]
	global_store_dwordx2 v253, v[250:251], s[90:91] nt
	v_cvt_scalef32_pk_fp8_f32 v250, v219, v223, v254
	v_cvt_scalef32_pk_fp8_f32 v251, v235, v239, v254
	v_cvt_scalef32_pk_fp8_f32 v250, v227, v231, v254 op_sel:[0,0,0,1]
	v_cvt_scalef32_pk_fp8_f32 v251, v243, v247, v254 op_sel:[0,0,0,1]
	global_store_dwordx2 v253, v[250:251], s[90:91] offset:2048 nt
	v_cvt_scalef32_pk_fp8_f32 v250, v220, v224, v254
	v_cvt_scalef32_pk_fp8_f32 v251, v236, v240, v254
	v_cvt_scalef32_pk_fp8_f32 v250, v228, v232, v254 op_sel:[0,0,0,1]
	v_cvt_scalef32_pk_fp8_f32 v251, v244, v248, v254 op_sel:[0,0,0,1]
	s_add_u32 s90, s90, 0x1000
	s_addc_u32 s91, s91, 0
	global_store_dwordx2 v253, v[250:251], s[90:91] nt
	v_cvt_scalef32_pk_fp8_f32 v250, v221, v225, v254
	v_cvt_scalef32_pk_fp8_f32 v251, v237, v241, v254
	v_cvt_scalef32_pk_fp8_f32 v250, v229, v233, v254 op_sel:[0,0,0,1]
	v_cvt_scalef32_pk_fp8_f32 v251, v245, v249, v254 op_sel:[0,0,0,1]
	global_store_dwordx2 v253, v[250:251], s[90:91] offset:2048 nt
	s_add_i32 s98, s98, 1
	s_mov_b32 s82, 0
	s_barrier
	s_setprio 1
	v_mfma_f32_16x16x128_f8f6f4 v[106:109], v[200:207], v[18:25], v[106:109]
	v_mfma_f32_16x16x128_f8f6f4 v[98:101], v[208:215], v[18:25], v[98:101]
	v_mfma_f32_16x16x128_f8f6f4 v[90:93], v[200:207], v[26:33], v[90:93]
	v_mfma_f32_16x16x128_f8f6f4 v[82:85], v[208:215], v[26:33], v[82:85]
	v_mfma_f32_16x16x128_f8f6f4 v[74:77], v[200:207], v[34:41], v[74:77]
	v_mfma_f32_16x16x128_f8f6f4 v[66:69], v[208:215], v[34:41], v[66:69]
	v_mfma_f32_16x16x128_f8f6f4 v[58:61], v[200:207], v[42:49], v[58:61]
	v_mfma_f32_16x16x128_f8f6f4 v[50:53], v[208:215], v[42:49], v[50:53]
	s_setprio 0
	s_add_i32 s29, s29, 2
	s_cmp_gt_u32 s29, 13
	s_barrier
	s_cbranch_scc1 .LBB0_853
	s_mov_b64 s[40:41], s[0:1]
	s_branch .LBB0_865
.LBB0_871:
	s_waitcnt vmcnt(0)
	s_cmp_eq_u32 s82, 2
	s_cbranch_scc0 .Le2_nofl
	v_cvt_scalef32_pk_fp8_f32 v250, v218, v222, v254
	v_cvt_scalef32_pk_fp8_f32 v251, v234, v238, v254
	v_cvt_scalef32_pk_fp8_f32 v250, v226, v230, v254 op_sel:[0,0,0,1]
	v_cvt_scalef32_pk_fp8_f32 v251, v242, v246, v254 op_sel:[0,0,0,1]
	global_store_dwordx2 v253, v[250:251], s[90:91] nt
	v_cvt_scalef32_pk_fp8_f32 v250, v219, v223, v254
	v_cvt_scalef32_pk_fp8_f32 v251, v235, v239, v254
	v_cvt_scalef32_pk_fp8_f32 v250, v227, v231, v254 op_sel:[0,0,0,1]
	v_cvt_scalef32_pk_fp8_f32 v251, v243, v247, v254 op_sel:[0,0,0,1]
	global_store_dwordx2 v253, v[250:251], s[90:91] offset:2048 nt
	v_cvt_scalef32_pk_fp8_f32 v250, v220, v224, v254
	v_cvt_scalef32_pk_fp8_f32 v251, v236, v240, v254
	v_cvt_scalef32_pk_fp8_f32 v250, v228, v232, v254 op_sel:[0,0,0,1]
	v_cvt_scalef32_pk_fp8_f32 v251, v244, v248, v254 op_sel:[0,0,0,1]
	s_add_u32 s90, s90, 0x1000
	s_addc_u32 s91, s91, 0
	global_store_dwordx2 v253, v[250:251], s[90:91] nt
	v_cvt_scalef32_pk_fp8_f32 v250, v221, v225, v254
	v_cvt_scalef32_pk_fp8_f32 v251, v237, v241, v254
	v_cvt_scalef32_pk_fp8_f32 v250, v229, v233, v254 op_sel:[0,0,0,1]
	v_cvt_scalef32_pk_fp8_f32 v251, v245, v249, v254 op_sel:[0,0,0,1]
	global_store_dwordx2 v253, v[250:251], s[90:91] offset:2048 nt
	s_add_i32 s98, s98, 1
	s_mov_b32 s82, 0
.Le2_nofl:
	s_cmpk_gt_u32 s61, 0xff
	s_cbranch_scc1 .LBB0_828
	s_barrier
	s_branch .LBB0_828
